# plus w_o epilogue counted waits and removal of dead bf16 H stores (phase 1, combine layer 0)
# speedup vs baseline: 1.0186x; 1.0070x over previous
; __device__ __forceinline__ void row_load_f32(Row& r, const float* p, int lane) {
; #pragma unroll
;     for (int j = 0; j < 4; ++j) { const f32x4 a = *(const f32x4*)(p + 512 * j + 8 * lane), b = *(const f32x4*)(p + 512 * j + 8 * lane + 4);
;         r.v[j][0] = a.x; r.v[j][1] = a.y; r.v[j][2] = a.z; r.v[j][3] = a.w; r.v[j][4] = b.x; r.v[j][5] = b.y; r.v[j][6] = b.z; r.v[j][7] = b.w; }
; }
; __device__ __forceinline__ void row_store_f32(const Row& r, float* p, int lane) {
; #pragma unroll
;     for (int j = 0; j < 4; ++j) { *(f32x4*)(p + 512 * j + 8 * lane) = (f32x4){r.v[j][0], r.v[j][1], r.v[j][2], r.v[j][3]}; *(f32x4*)(p + 512 * j + 8 * lane + 4) = (f32x4){r.v[j][4], r.v[j][5], r.v[j][6], r.v[j][7]}; }
; }
; __device__ __forceinline__ void row_store_bf16(const Row& r, bf16* p, int lane) {
; #pragma unroll
;     for (int j = 0; j < 4; ++j) { u32x4 o; o.x = cvtpk(r.v[j][0], r.v[j][1]); o.y = cvtpk(r.v[j][2], r.v[j][3]); o.z = cvtpk(r.v[j][4], r.v[j][5]); o.w = cvtpk(r.v[j][6], r.v[j][7]); *(u32x4*)(p + 512 * j + 8 * lane) = o; }
; }
; __device__ __forceinline__ float row_rstd(const Row& r) {
;     float s = 0.f;
; #pragma unroll
;     for (int j = 0; j < 4; ++j)
; #pragma unroll
;         for (int q = 0; q < 8; ++q) s += r.v[j][q] * r.v[j][q];
;     return rsqrtf(wave_sum(s) * (1.0f / DM) + EPS);
; }
; __device__ __forceinline__ void row_norm_mod_store(const Row& x, const float* g, ModPtr sh, ModPtr sc, bf16* hrow, int lane, unsigned char* h8row = nullptr) {
;     const float rstd = row_rstd(x);
;     Row o;
; #pragma unroll
;     for (int j = 0; j < 4; ++j) { const int c0 = 512 * j + 8 * lane;
; #pragma unroll
;         for (int q4 = 0; q4 < 2; ++q4) { const int c = c0 + 4 * q4;
;             const f32x4 gv = *(const f32x4*)(g + c), sa = *(const f32x4*)(sh.acc + c), ca = *(const f32x4*)(sc.acc + c);
; #pragma unroll
;             for (int q = 0; q < 4; ++q) o.v[j][4 * q4 + q] = (x.v[j][4 * q4 + q] * rstd * gv[q]) * (1.0f + ca[q]) + sa[q]; }
;         asm volatile("" ::: "memory"); }
;     if (hrow) row_store_bf16(o, hrow, lane);
;     if (h8row) {
; #pragma unroll
;         for (int j = 0; j < 4; ++j) *(u32x2*)(h8row + 512 * j + 8 * lane) = pack8_fp8((f32x4){o.v[j][0], o.v[j][1], o.v[j][2], o.v[j][3]}, (f32x4){o.v[j][4], o.v[j][5], o.v[j][6], o.v[j][7]}); }
; }
.LBB0_471:
	global_load_dwordx4 v[26:29], v[48:49], off offset:-4080
	global_load_dwordx4 v[30:33], v[48:49], off offset:-4096
	global_load_dwordx4 v[18:21], v[48:49], off offset:-2032
	global_load_dwordx4 v[22:25], v[48:49], off offset:-2048
	global_load_dwordx4 v[10:13], v[48:49], off offset:16
	global_load_dwordx4 v[14:17], v[48:49], off
	global_load_dwordx4 v[2:5], v[48:49], off offset:2064
	global_load_dwordx4 v[6:9], v[48:49], off offset:2048
	global_load_dwordx4 v[34:37], v[42:43], off offset:16
	global_load_dwordx4 v[38:41], v[42:43], off
	s_ashr_i32 s14, s0, 31
	s_lshr_b32 s14, s14, 20
	s_add_i32 s14, s0, s14
	s_ashr_i32 s14, s14, 12
	s_mul_hi_i32 s15, s14, 0xc000
	s_mul_i32 s14, s14, 0xc000
	v_lshl_add_u64 v[62:63], s[2:3], 0, v[52:53]
	s_add_u32 s14, s10, s14
	v_add_co_u32_e32 v156, vcc, s12, v62
	s_addc_u32 s15, s11, s15
	v_lshl_add_u64 v[68:69], s[2:3], 0, v[50:51]
	v_addc_co_u32_e32 v157, vcc, 0, v63, vcc
	s_add_u32 s16, s14, 0x2000
	v_add_co_u32_e32 v62, vcc, s13, v68
	s_addc_u32 s17, s15, 0
	s_nop 0
	v_addc_co_u32_e32 v63, vcc, 0, v69, vcc
	global_load_dwordx4 v[68:71], v64, s[14:15] offset:16
	global_load_dwordx4 v[72:75], v64, s[14:15]
	global_load_dwordx4 v[76:79], v64, s[16:17]
	global_load_dwordx4 v[80:83], v64, s[16:17] offset:16
	global_load_dwordx4 v[84:87], v65, s[16:17]
	global_load_dwordx4 v[88:91], v65, s[16:17] offset:16
	global_load_dwordx4 v[92:95], v[42:43], off offset:2064
	global_load_dwordx4 v[96:99], v[42:43], off offset:2048
	global_load_dwordx4 v[100:103], v64, s[14:15] offset:2064
	global_load_dwordx4 v[104:107], v64, s[14:15] offset:2048
	global_load_dwordx4 v[108:111], v66, s[16:17]
	global_load_dwordx4 v[112:115], v66, s[16:17] offset:16
	global_load_dwordx4 v[116:119], v[44:45], off offset:16
	global_load_dwordx4 v[120:123], v[44:45], off
	global_load_dwordx4 v[124:127], v66, s[14:15] offset:16
	global_load_dwordx4 v[128:131], v66, s[14:15]
	global_load_dwordx4 v[132:135], v67, s[16:17]
	global_load_dwordx4 v[136:139], v67, s[16:17] offset:16
	global_load_dwordx4 v[140:143], v[46:47], off offset:16
	global_load_dwordx4 v[144:147], v[46:47], off
	global_load_dwordx4 v[148:151], v67, s[14:15] offset:16
	global_load_dwordx4 v[152:155], v67, s[14:15]
	v_mov_b32_e32 v54, 0
	v_mov_b32_e32 v55, 0
	v_mov_b32_e32 v56, 0
	v_mov_b32_e32 v57, 0
	v_mov_b32_e32 v58, 0
	v_mov_b32_e32 v59, 0
	v_mov_b32_e32 v60, 0
	v_mov_b32_e32 v61, 0
	s_add_i32 s18, s0, 0x800
	v_lshl_add_u64 v[48:49], v[48:49], 0, s[4:5]
	v_lshl_add_u64 v[50:51], v[50:51], 0, s[6:7]
	v_lshl_add_u64 v[52:53], v[52:53], 0, s[8:9]
	s_cmpk_lt_i32 s0, 0x1800
	s_mov_b32 s0, s18
	s_waitcnt vmcnt(30)
	v_mul_f32_e32 v164, v31, v31
	v_fmac_f32_e32 v164, v30, v30
	v_fmac_f32_e32 v164, v32, v32
	v_fmac_f32_e32 v164, v33, v33
	v_fmac_f32_e32 v164, v26, v26
	v_fmac_f32_e32 v164, v27, v27
	v_fmac_f32_e32 v164, v28, v28
	v_fmac_f32_e32 v164, v29, v29
	s_waitcnt vmcnt(28)
	v_fmac_f32_e32 v164, v22, v22
	v_fmac_f32_e32 v164, v23, v23
	v_fmac_f32_e32 v164, v24, v24
	v_fmac_f32_e32 v164, v25, v25
	v_fmac_f32_e32 v164, v18, v18
	v_fmac_f32_e32 v164, v19, v19
	v_fmac_f32_e32 v164, v20, v20
	v_fmac_f32_e32 v164, v21, v21
	s_waitcnt vmcnt(26)
	v_fmac_f32_e32 v164, v14, v14
	v_fmac_f32_e32 v164, v15, v15
	v_fmac_f32_e32 v164, v16, v16
	v_fmac_f32_e32 v164, v17, v17
	v_fmac_f32_e32 v164, v10, v10
	v_fmac_f32_e32 v164, v11, v11
	v_fmac_f32_e32 v164, v12, v12
	v_fmac_f32_e32 v164, v13, v13
	s_waitcnt vmcnt(24)
	v_fmac_f32_e32 v164, v6, v6
	v_pk_mul_f32 v[158:159], v[8:9], v[8:9]
	v_fmac_f32_e32 v164, v7, v7
	v_pk_mul_f32 v[162:163], v[2:3], v[2:3]
	v_pk_mul_f32 v[160:161], v[4:5], v[4:5]
	s_waitcnt vmcnt(19)
	v_add_f32_e32 v165, 1.0, v76
	v_add_f32_e32 v76, v158, v164
	v_add_f32_e32 v76, v159, v76
	v_add_f32_e32 v76, v162, v76
	v_add_f32_e32 v76, v163, v76
	v_add_f32_e32 v76, v160, v76
	v_add_f32_e32 v76, v161, v76
	v_add_f32_e32 v166, 1.0, v77
	s_waitcnt vmcnt(18)
	v_add_f32_e32 v80, 1.0, v80
	v_add_f32_dpp v76, v76, v76 quad_perm:[1,0,3,2] row_mask:0xf bank_mask:0xf bound_ctrl:1
	v_add_f32_e32 v81, 1.0, v81
	s_waitcnt vmcnt(17)
	v_add_f32_e32 v84, 1.0, v84
	v_add_f32_dpp v76, v76, v76 quad_perm:[2,3,0,1] row_mask:0xf bank_mask:0xf bound_ctrl:1
	v_add_f32_e32 v85, 1.0, v85
	s_waitcnt vmcnt(16)
	v_add_f32_e32 v88, 1.0, v88
	v_add_f32_dpp v76, v76, v76 row_half_mirror row_mask:0xf bank_mask:0xf bound_ctrl:1
	v_add_f32_e32 v89, 1.0, v89
	s_waitcnt vmcnt(11)
	v_add_f32_e32 v108, 1.0, v108
	v_add_f32_dpp v76, v76, v76 row_mirror row_mask:0xf bank_mask:0xf bound_ctrl:1
	v_add_f32_e32 v109, 1.0, v109
	v_readlane_b32 s16, v76, 16
	v_readlane_b32 s17, v76, 48
	v_readlane_b32 s14, v76, 0
	v_readlane_b32 s15, v76, 32
	v_mov_b32_e32 v76, s16
	v_mov_b32_e32 v77, s17
	v_pk_add_f32 v[76:77], s[14:15], v[76:77]
	s_waitcnt vmcnt(10)
	v_add_f32_e32 v112, 1.0, v112
	v_add_f32_e32 v76, v76, v77
	v_fmamk_f32 v76, v76, 0x3a000000, v1
	v_mul_f32_e32 v77, 0x4b800000, v76
	v_cmp_gt_f32_e32 vcc, s1, v76
	v_add_f32_e32 v113, 1.0, v113
	v_add_f32_e32 v115, 1.0, v115
	v_cndmask_b32_e32 v76, v76, v77, vcc
	v_rsq_f32_e32 v76, v76
	s_waitcnt vmcnt(5)
; __device__ __forceinline__ void row_norm_mod_store(const Row& x, const float* g, ModPtr sh, ModPtr sc, bf16* hrow, int lane, unsigned char* h8row = nullptr) {
;     const float rstd = row_rstd(x);
;     Row o;
; #pragma unroll
;     for (int j = 0; j < 4; ++j) { const int c0 = 512 * j + 8 * lane;
; #pragma unroll
;         for (int q4 = 0; q4 < 2; ++q4) { const int c = c0 + 4 * q4;
;             const f32x4 gv = *(const f32x4*)(g + c), sa = *(const f32x4*)(sh.acc + c), ca = *(const f32x4*)(sc.acc + c);
; #pragma unroll
;             for (int q = 0; q < 4; ++q) o.v[j][4 * q4 + q] = (x.v[j][4 * q4 + q] * rstd * gv[q]) * (1.0f + ca[q]) + sa[q]; }
;         asm volatile("" ::: "memory"); }
;     if (hrow) row_store_bf16(o, hrow, lane);
;     if (h8row) {
; #pragma unroll
;         for (int j = 0; j < 4; ++j) *(u32x2*)(h8row + 512 * j + 8 * lane) = pack8_fp8((f32x4){o.v[j][0], o.v[j][1], o.v[j][2], o.v[j][3]}, (f32x4){o.v[j][4], o.v[j][5], o.v[j][6], o.v[j][7]}); }
; }
	v_add_f32_e32 v132, 1.0, v132
	v_add_f32_e32 v133, 1.0, v133
	v_add_f32_e32 v135, 1.0, v135
	v_mul_f32_e32 v77, 0x45800000, v76
	v_cndmask_b32_e32 v76, v76, v77, vcc
	v_mul_f32_e32 v30, v30, v76
	v_mul_f32_e32 v31, v31, v76
	v_mul_f32_e32 v26, v26, v76
	v_mul_f32_e32 v27, v27, v76
	v_mul_f32_e32 v22, v22, v76
	v_mul_f32_e32 v23, v23, v76
	v_mul_f32_e32 v18, v18, v76
	v_mul_f32_e32 v19, v19, v76
	v_mul_f32_e32 v30, v38, v30
	v_mul_f32_e32 v31, v39, v31
	v_mul_f32_e32 v26, v34, v26
	v_mul_f32_e32 v27, v35, v27
	v_mul_f32_e32 v14, v14, v76
	v_mul_f32_e32 v15, v15, v76
	v_mul_f32_e32 v10, v10, v76
	v_mul_f32_e32 v11, v11, v76
	v_mul_f32_e32 v22, v96, v22
	v_mul_f32_e32 v23, v97, v23
	v_mul_f32_e32 v18, v18, v92
	v_mul_f32_e32 v19, v19, v93
	v_fma_f32 v30, v165, v30, v72
	v_fma_f32 v31, v166, v31, v73
	v_fma_f32 v26, v80, v26, v68
	v_fma_f32 v27, v81, v27, v69
	v_mul_f32_e32 v13, v13, v76
	v_mul_f32_e32 v6, v6, v76
	v_mul_f32_e32 v7, v7, v76
	v_mul_f32_e32 v9, v9, v76
	v_mul_f32_e32 v2, v2, v76
	v_mul_f32_e32 v3, v3, v76
	v_mul_f32_e32 v14, v14, v120
	v_mul_f32_e32 v15, v15, v121
	v_mul_f32_e32 v10, v10, v116
	v_mul_f32_e32 v11, v11, v117
	v_fma_f32 v22, v22, v84, v104
	v_fma_f32 v23, v23, v85, v105
	v_fma_f32 v18, v18, v88, v100
	v_fma_f32 v19, v19, v89, v101
	v_cvt_pk_fp8_f32 v54, v30, v31
	v_cvt_pk_fp8_f32 v55, v26, v27
	s_waitcnt vmcnt(4)
	v_add_f32_e32 v136, 1.0, v136
	v_add_f32_e32 v137, 1.0, v137
	v_mul_f32_e32 v32, v32, v76
	v_mul_f32_e32 v33, v33, v76
	v_mul_f32_e32 v28, v28, v76
	v_mul_f32_e32 v29, v29, v76
	v_mul_f32_e32 v13, v13, v119
	s_waitcnt vmcnt(2)
	v_mul_f32_e32 v6, v6, v144
	v_mul_f32_e32 v7, v7, v145
	v_mul_f32_e32 v9, v9, v147
	v_mul_f32_e32 v2, v2, v140
	v_mul_f32_e32 v3, v3, v141
	v_fma_f32 v14, v14, v108, v128
	v_fma_f32 v15, v15, v109, v129
	v_fma_f32 v10, v10, v112, v124
	v_fma_f32 v11, v11, v113, v125
	v_cvt_pk_fp8_f32 v56, v22, v23
	v_cvt_pk_fp8_f32 v57, v18, v19
	v_add_f32_e32 v78, 1.0, v78
	v_add_f32_e32 v79, 1.0, v79
	v_add_f32_e32 v82, 1.0, v82
	v_add_f32_e32 v83, 1.0, v83
	v_mul_f32_e32 v24, v24, v76
	v_mul_f32_e32 v25, v25, v76
	v_mul_f32_e32 v20, v20, v76
	v_mul_f32_e32 v21, v21, v76
	v_mul_f32_e32 v32, v40, v32
	v_mul_f32_e32 v33, v41, v33
	v_mul_f32_e32 v28, v36, v28
	v_mul_f32_e32 v29, v37, v29
	v_fmac_f32_e32 v127, v13, v115
	s_waitcnt vmcnt(0)
	v_fma_f32 v6, v6, v132, v152
	v_fma_f32 v7, v7, v133, v153
	v_fmac_f32_e32 v155, v9, v135
	v_fma_f32 v9, v2, v136, v148
	v_fma_f32 v13, v3, v137, v149
	v_cvt_pk_fp8_f32 v58, v14, v15
	v_cvt_pk_fp8_f32 v59, v10, v11
	v_add_f32_e32 v86, 1.0, v86
	v_add_f32_e32 v87, 1.0, v87
	v_add_f32_e32 v90, 1.0, v90
	v_add_f32_e32 v91, 1.0, v91
	v_mul_f32_e32 v16, v16, v76
	v_mul_f32_e32 v17, v17, v76
	v_mul_f32_e32 v12, v12, v76
	v_mul_f32_e32 v4, v4, v76
	v_mul_f32_e32 v5, v5, v76
	v_mul_f32_e32 v24, v98, v24
	v_mul_f32_e32 v25, v99, v25
	v_mul_f32_e32 v20, v20, v94
	v_mul_f32_e32 v21, v21, v95
	v_fma_f32 v32, v78, v32, v74
	v_fmac_f32_e32 v75, v79, v33
	v_fma_f32 v28, v82, v28, v70
	v_fmac_f32_e32 v71, v83, v29
	v_cvt_pk_fp8_f32 v60, v6, v7
	v_cvt_pk_fp8_f32 v61, v9, v13
	v_add_f32_e32 v110, 1.0, v110
	v_add_f32_e32 v111, 1.0, v111
	v_add_f32_e32 v114, 1.0, v114
	v_add_f32_e32 v138, 1.0, v138
	v_add_f32_e32 v139, 1.0, v139
	v_mul_f32_e32 v8, v8, v76
	v_mul_f32_e32 v16, v16, v122
	v_mul_f32_e32 v17, v17, v123
	v_mul_f32_e32 v12, v12, v118
	v_mul_f32_e32 v4, v4, v142
	v_mul_f32_e32 v5, v5, v143
	v_fma_f32 v24, v24, v86, v106
	v_fmac_f32_e32 v107, v25, v87
	v_fma_f32 v20, v20, v90, v102
	v_fmac_f32_e32 v103, v21, v91
	v_cvt_pk_fp8_f32 v54, v32, v75 op_sel:[0,0,1]
	v_cvt_pk_fp8_f32 v55, v28, v71 op_sel:[0,0,1]
	v_add_f32_e32 v134, 1.0, v134
	v_mul_f32_e32 v8, v8, v146
	v_fma_f32 v16, v16, v110, v130
	v_fmac_f32_e32 v131, v17, v111
	v_fma_f32 v12, v12, v114, v126
	v_fma_f32 v17, v4, v138, v150
	v_fmac_f32_e32 v151, v5, v139
	v_cvt_pk_bf16_f32 v2, v30, v31
	v_cvt_pk_bf16_f32 v3, v32, v75
	v_cvt_pk_bf16_f32 v4, v26, v27
	v_cvt_pk_bf16_f32 v5, v28, v71
	v_cvt_pk_fp8_f32 v56, v24, v107 op_sel:[0,0,1]
	v_cvt_pk_fp8_f32 v57, v20, v103 op_sel:[0,0,1]
	v_fma_f32 v8, v8, v134, v154
	v_cvt_pk_fp8_f32 v58, v16, v131 op_sel:[0,0,1]
	v_cvt_pk_fp8_f32 v59, v12, v127 op_sel:[0,0,1]
	v_cvt_pk_bf16_f32 v2, v22, v23
	v_cvt_pk_bf16_f32 v3, v24, v107
	v_cvt_pk_bf16_f32 v4, v18, v19
	v_cvt_pk_bf16_f32 v5, v20, v103
	v_cvt_pk_fp8_f32 v60, v8, v155 op_sel:[0,0,1]
	v_cvt_pk_fp8_f32 v61, v17, v151 op_sel:[0,0,1]
	v_cvt_pk_bf16_f32 v2, v14, v15
	v_cvt_pk_bf16_f32 v3, v16, v131
	v_cvt_pk_bf16_f32 v4, v10, v11
	v_cvt_pk_bf16_f32 v5, v12, v127
	s_nop 1
	v_cvt_pk_bf16_f32 v2, v6, v7
	v_cvt_pk_bf16_f32 v3, v8, v155
	v_cvt_pk_bf16_f32 v4, v9, v13
	v_cvt_pk_bf16_f32 v5, v17, v151
	global_store_dwordx2 v[62:63], v[54:55], off
	global_store_dwordx2 v[62:63], v[56:57], off offset:512
	global_store_dwordx2 v[62:63], v[58:59], off offset:1024
	global_store_dwordx2 v[62:63], v[60:61], off offset:1536
	s_cbranch_scc1 .LBB0_471

; __device__ __forceinline__ u32x4 pack8(const f32x4 a, const f32x4 b) { u32x4 w; w.x = cvtpk(a[0], a[1]); w.y = cvtpk(a[2], a[3]); w.z = cvtpk(b[0], b[1]); w.w = cvtpk(b[2], b[3]); return w; }
; __device__ __forceinline__ void unpack8(const u32x4 w, f32x4& a, f32x4& b) { a = (f32x4){bflo(w.x), bfhi(w.x), bflo(w.y), bfhi(w.y)}; b = (f32x4){bflo(w.z), bfhi(w.z), bflo(w.w), bfhi(w.w)}; }
;     __device__ __forceinline__ void load(Regs& r, const pg::Unit& u, int g, int wr, int wc, int fr, int fq) const {
;         EPI_G(g)
; #pragma unroll
;         for (int bj = 0; bj < 2; ++bj) { const int col = u.pn * 256 + bj * 128 + wc * 32 + 8 * fq; r.p[bj] = *(const u32x4*)(P + (size_t)row * NINP + PC_LA + col); r.q[bj] = *(const u32x4*)(M1 + (size_t)row * DM + col); }
;     }
;     __device__ __forceinline__ void finish(const Regs& r, const pg::Acc& acc, const pg::Unit& u, int g, int wr, int wc, int fr, int fq) const {
;         EPI_G(g)
; #pragma unroll
;         for (int bj = 0; bj < 2; ++bj) { const int col = u.pn * 256 + bj * 128 + wc * 32 + 8 * fq; f32x4 g0, g1, a0, a1; unpack8(r.p[bj], g0, g1); unpack8(r.q[bj], a0, a1);
;             const f32x4 m0 = acc[ai][bj][m][0] * isc * g0 + a0, m1v = acc[ai][bj][m][1] * isc * g1 + a1;
;             if (FP8_WOUT) *(u32x2*)(MIX8 + (size_t)row * DM + col) = pack8_fp8(m0, m1v); else *(u32x4*)(MIX + (size_t)row * DM + col) = pack8(m0, m1v); }
;     }
.LBB0_1181:
	s_lshl_b32 s24, s33, 8
	v_add_u32_e32 v24, s24, v1
	v_ashrrev_i32_e32 v25, 31, v24
	v_lshlrev_b64 v[4:5], 14, v[24:25]
	v_lshl_or_b32 v2, s22, 8, v221
	v_lshl_add_u64 v[4:5], s[6:7], 0, v[4:5]
	v_ashrrev_i32_e32 v3, 31, v2
	v_lshl_add_u64 v[16:17], v[4:5], 0, s[14:15]
	v_lshlrev_b64 v[4:5], 1, v[2:3]
	v_lshl_add_u64 v[6:7], v[16:17], 0, v[4:5]
	global_load_dwordx4 v[8:11], v[6:7], off
	v_lshlrev_b64 v[6:7], 12, v[24:25]
	v_lshl_add_u64 v[6:7], s[8:9], 0, v[6:7]
	v_lshl_add_u64 v[20:21], v[6:7], 0, v[4:5]
	v_or_b32_e32 v6, 0x80, v2
	v_ashrrev_i32_e32 v7, 31, v6
	global_load_dwordx4 v[12:15], v[20:21], off
	v_lshlrev_b64 v[6:7], 1, v[6:7]
	v_lshl_add_u64 v[16:17], v[16:17], 0, v[6:7]
	global_load_dwordx4 v[16:19], v[16:17], off
	s_nop 0
	global_load_dwordx4 v[20:23], v[20:21], off offset:256
	s_or_b32 s25, s24, 16
	v_add_u32_e32 v58, s25, v1
	v_ashrrev_i32_e32 v59, 31, v58
	v_lshlrev_b64 v[60:61], 11, v[24:25]
	v_lshlrev_b64 v[24:25], 14, v[58:59]
	v_lshl_add_u64 v[24:25], s[6:7], 0, v[24:25]
	v_lshl_add_u64 v[28:29], v[24:25], 0, s[14:15]
	v_lshl_add_u64 v[24:25], v[28:29], 0, v[4:5]
	v_lshlrev_b64 v[30:31], 12, v[58:59]
	global_load_dwordx4 v[24:27], v[24:25], off
	v_lshl_add_u64 v[30:31], s[8:9], 0, v[30:31]
	v_lshl_add_u64 v[36:37], v[30:31], 0, v[4:5]
	v_lshl_add_u64 v[32:33], v[28:29], 0, v[6:7]
	global_load_dwordx4 v[28:31], v[36:37], off
	s_nop 0
	global_load_dwordx4 v[32:35], v[32:33], off
	s_nop 0
	global_load_dwordx4 v[36:39], v[36:37], off offset:256
	v_pk_mul_f32 v[40:41], v[188:189], s[16:17] op_sel_hi:[1,0]
	v_pk_mul_f32 v[42:43], v[186:187], s[16:17] op_sel_hi:[1,0]
	v_pk_mul_f32 v[54:55], v[178:179], s[16:17] op_sel_hi:[1,0]
	v_pk_mul_f32 v[44:45], v[184:185], s[16:17] op_sel_hi:[1,0]
	v_pk_mul_f32 v[46:47], v[182:183], s[16:17] op_sel_hi:[1,0]
	v_mov_b32_e32 v48, v199
	v_mov_b32_e32 v49, v199
	v_pk_mul_f32 v[50:51], v[192:193], s[16:17] op_sel_hi:[1,0]
	v_pk_mul_f32 v[52:53], v[190:191], s[16:17] op_sel_hi:[1,0]
	v_mov_b32_e32 v56, v199
	v_mov_b32_e32 v57, v199
	s_or_b32 s22, s24, 32
	s_or_b32 s19, s24, 48
	s_andn2_b64 vcc, exec, s[2:3]
	s_mov_b64 s[2:3], -1
	s_waitcnt vmcnt(0)
	v_lshlrev_b32_e32 v62, 16, v8
	v_and_b32_e32 v63, 0xffff0000, v8
	v_lshlrev_b32_e32 v8, 16, v9
	v_and_b32_e32 v9, 0xffff0000, v9
	v_lshlrev_b32_e32 v64, 16, v10
	v_and_b32_e32 v65, 0xffff0000, v10
	v_lshlrev_b32_e32 v178, 16, v12
	v_and_b32_e32 v179, 0xffff0000, v12
	v_lshlrev_b32_e32 v12, 16, v13
	v_and_b32_e32 v13, 0xffff0000, v13
	v_lshlrev_b32_e32 v10, 16, v11
	v_and_b32_e32 v11, 0xffff0000, v11
	v_lshlrev_b32_e32 v182, 16, v14
	v_and_b32_e32 v183, 0xffff0000, v14
	v_lshlrev_b32_e32 v14, 16, v15
	v_and_b32_e32 v15, 0xffff0000, v15
	v_pk_fma_f32 v[8:9], v[40:41], v[8:9], v[12:13]
	v_pk_fma_f32 v[12:13], v[42:43], v[62:63], v[178:179]
	v_lshlrev_b32_e32 v184, 16, v16
	v_and_b32_e32 v185, 0xffff0000, v16
	v_lshlrev_b32_e32 v16, 16, v17
	v_and_b32_e32 v17, 0xffff0000, v17
	v_lshlrev_b32_e32 v186, 16, v18
	v_and_b32_e32 v187, 0xffff0000, v18
	v_lshlrev_b32_e32 v188, 16, v20
	v_and_b32_e32 v189, 0xffff0000, v20
	v_lshlrev_b32_e32 v20, 16, v21
	v_and_b32_e32 v21, 0xffff0000, v21
	v_lshlrev_b32_e32 v190, 16, v22
	v_and_b32_e32 v191, 0xffff0000, v22
	v_pk_fma_f32 v[10:11], v[44:45], v[10:11], v[14:15]
	v_pk_fma_f32 v[14:15], v[46:47], v[64:65], v[182:183]
	v_cvt_pk_fp8_f32 v48, v12, v13
	v_pk_fma_f32 v[16:17], v[50:51], v[16:17], v[20:21]
	v_pk_fma_f32 v[20:21], v[52:53], v[184:185], v[188:189]
	v_pk_fma_f32 v[40:41], v[54:55], v[186:187], v[190:191]
	v_cvt_pk_fp8_f32 v49, v14, v15
	v_cvt_pk_fp8_f32 v56, v20, v21
	v_cvt_pk_fp8_f32 v57, v40, v41
	v_lshlrev_b32_e32 v18, 16, v19
	v_and_b32_e32 v19, 0xffff0000, v19
	v_lshlrev_b32_e32 v22, 16, v23
	v_and_b32_e32 v23, 0xffff0000, v23
	v_cvt_pk_fp8_f32 v48, v8, v9 op_sel:[0,0,1]
	v_pk_mul_f32 v[8:9], v[180:181], s[16:17] op_sel_hi:[1,0]
	v_cvt_pk_fp8_f32 v49, v10, v11 op_sel:[0,0,1]
	v_pk_fma_f32 v[8:9], v[8:9], v[18:19], v[22:23]
	v_cvt_pk_fp8_f32 v56, v16, v17 op_sel:[0,0,1]
	v_cvt_pk_fp8_f32 v57, v8, v9 op_sel:[0,0,1]
	v_lshl_add_u64 v[8:9], s[10:11], 0, v[60:61]
	v_add_u32_e32 v40, s22, v1
	v_lshl_add_u64 v[8:9], v[8:9], 0, v[2:3]
	v_ashrrev_i32_e32 v41, 31, v40
	global_store_dwordx2 v[8:9], v[48:49], off
	global_store_dwordx2 v[8:9], v[56:57], off offset:128
	v_lshlrev_b64 v[8:9], 12, v[40:41]
	v_lshl_add_u64 v[8:9], s[8:9], 0, v[8:9]
	v_lshl_add_u64 v[12:13], v[8:9], 0, v[4:5]
	v_lshlrev_b64 v[8:9], 14, v[40:41]
	v_lshl_add_u64 v[8:9], s[6:7], 0, v[8:9]
	v_lshl_add_u64 v[16:17], v[8:9], 0, s[14:15]
	v_lshl_add_u64 v[18:19], v[16:17], 0, v[6:7]
	v_lshl_add_u64 v[20:21], v[16:17], 0, v[4:5]
	global_load_dwordx4 v[8:11], v[12:13], off offset:256
	s_nop 0
	global_load_dwordx4 v[12:15], v[12:13], off
	s_nop 0
	global_load_dwordx4 v[16:19], v[18:19], off
	s_nop 0
	global_load_dwordx4 v[20:23], v[20:21], off
	v_lshlrev_b32_e32 v44, 16, v24
	v_and_b32_e32 v45, 0xffff0000, v24
	v_lshlrev_b32_e32 v24, 16, v25
	v_and_b32_e32 v25, 0xffff0000, v25
	v_lshlrev_b32_e32 v48, 16, v28
	v_and_b32_e32 v49, 0xffff0000, v28
	v_lshlrev_b32_e32 v28, 16, v29
	v_and_b32_e32 v29, 0xffff0000, v29
	v_pk_mul_f32 v[52:53], v[172:173], s[16:17] op_sel_hi:[1,0]
	v_pk_mul_f32 v[54:55], v[170:171], s[16:17] op_sel_hi:[1,0]
	v_lshlrev_b32_e32 v46, 16, v26
	v_and_b32_e32 v47, 0xffff0000, v26
	v_lshlrev_b32_e32 v50, 16, v30
	v_and_b32_e32 v51, 0xffff0000, v30
	v_pk_fma_f32 v[24:25], v[52:53], v[24:25], v[28:29]
	v_pk_fma_f32 v[28:29], v[54:55], v[44:45], v[48:49]
	v_pk_mul_f32 v[44:45], v[162:163], s[16:17] op_sel_hi:[1,0]
	v_lshlrev_b32_e32 v26, 16, v27
	v_pk_fma_f32 v[44:45], v[44:45], v[46:47], v[50:51]
	v_mov_b32_e32 v46, v199
; __device__ __forceinline__ u32x4 pack8(const f32x4 a, const f32x4 b) { u32x4 w; w.x = cvtpk(a[0], a[1]); w.y = cvtpk(a[2], a[3]); w.z = cvtpk(b[0], b[1]); w.w = cvtpk(b[2], b[3]); return w; }
; __device__ __forceinline__ void unpack8(const u32x4 w, f32x4& a, f32x4& b) { a = (f32x4){bflo(w.x), bfhi(w.x), bflo(w.y), bfhi(w.y)}; b = (f32x4){bflo(w.z), bfhi(w.z), bflo(w.w), bfhi(w.w)}; }
;     __device__ __forceinline__ void load(Regs& r, const pg::Unit& u, int g, int wr, int wc, int fr, int fq) const {
;         EPI_G(g)
; #pragma unroll
;         for (int bj = 0; bj < 2; ++bj) { const int col = u.pn * 256 + bj * 128 + wc * 32 + 8 * fq; r.p[bj] = *(const u32x4*)(P + (size_t)row * NINP + PC_LA + col); r.q[bj] = *(const u32x4*)(M1 + (size_t)row * DM + col); }
;     }
;     __device__ __forceinline__ void finish(const Regs& r, const pg::Acc& acc, const pg::Unit& u, int g, int wr, int wc, int fr, int fq) const {
;         EPI_G(g)
; #pragma unroll
;         for (int bj = 0; bj < 2; ++bj) { const int col = u.pn * 256 + bj * 128 + wc * 32 + 8 * fq; f32x4 g0, g1, a0, a1; unpack8(r.p[bj], g0, g1); unpack8(r.q[bj], a0, a1);
;             const f32x4 m0 = acc[ai][bj][m][0] * isc * g0 + a0, m1v = acc[ai][bj][m][1] * isc * g1 + a1;
;             if (FP8_WOUT) *(u32x2*)(MIX8 + (size_t)row * DM + col) = pack8_fp8(m0, m1v); else *(u32x4*)(MIX + (size_t)row * DM + col) = pack8(m0, m1v); }
;     }
	v_mov_b32_e32 v47, v199
	v_cvt_pk_fp8_f32 v46, v28, v29
	v_cvt_pk_fp8_f32 v47, v44, v45
	v_and_b32_e32 v27, 0xffff0000, v27
	v_lshlrev_b32_e32 v30, 16, v31
	v_and_b32_e32 v31, 0xffff0000, v31
	v_pk_mul_f32 v[28:29], v[164:165], s[16:17] op_sel_hi:[1,0]
	v_cvt_pk_fp8_f32 v46, v24, v25 op_sel:[0,0,1]
	v_pk_fma_f32 v[26:27], v[28:29], v[26:27], v[30:31]
	v_lshlrev_b32_e32 v24, 16, v32
	v_cvt_pk_fp8_f32 v47, v26, v27 op_sel:[0,0,1]
	v_and_b32_e32 v25, 0xffff0000, v32
	v_lshlrev_b32_e32 v26, 16, v33
	v_and_b32_e32 v27, 0xffff0000, v33
	v_lshlrev_b32_e32 v32, 16, v36
	v_and_b32_e32 v33, 0xffff0000, v36
	v_pk_mul_f32 v[48:49], v[174:175], s[16:17] op_sel_hi:[1,0]
	v_lshlrev_b32_e32 v28, 16, v34
	v_and_b32_e32 v29, 0xffff0000, v34
	v_lshlrev_b32_e32 v30, 16, v35
	v_and_b32_e32 v31, 0xffff0000, v35
	v_lshlrev_b32_e32 v34, 16, v37
	v_and_b32_e32 v35, 0xffff0000, v37
	v_lshlrev_b32_e32 v36, 16, v38
	v_and_b32_e32 v37, 0xffff0000, v38
	v_pk_fma_f32 v[24:25], v[48:49], v[24:25], v[32:33]
	v_pk_mul_f32 v[32:33], v[166:167], s[16:17] op_sel_hi:[1,0]
	v_lshlrev_b32_e32 v38, 16, v39
	v_pk_fma_f32 v[28:29], v[32:33], v[28:29], v[36:37]
	v_mov_b32_e32 v32, v199
	v_mov_b32_e32 v33, v199
	v_cvt_pk_fp8_f32 v32, v24, v25
	v_cvt_pk_fp8_f32 v33, v28, v29
	v_and_b32_e32 v39, 0xffff0000, v39
	v_pk_mul_f32 v[44:45], v[176:177], s[16:17] op_sel_hi:[1,0]
	v_pk_mul_f32 v[24:25], v[168:169], s[16:17] op_sel_hi:[1,0]
	v_pk_fma_f32 v[26:27], v[44:45], v[26:27], v[34:35]
	v_pk_fma_f32 v[24:25], v[24:25], v[30:31], v[38:39]
	v_lshlrev_b64 v[42:43], 11, v[58:59]
	v_cvt_pk_fp8_f32 v32, v26, v27 op_sel:[0,0,1]
	v_cvt_pk_fp8_f32 v33, v24, v25 op_sel:[0,0,1]
	v_lshl_add_u64 v[24:25], s[10:11], 0, v[42:43]
	v_add_u32_e32 v42, s19, v1
	v_lshl_add_u64 v[24:25], v[24:25], 0, v[2:3]
	v_ashrrev_i32_e32 v43, 31, v42
	global_store_dwordx2 v[24:25], v[46:47], off
	global_store_dwordx2 v[24:25], v[32:33], off offset:128
	v_lshlrev_b64 v[24:25], 14, v[42:43]
	v_lshl_add_u64 v[24:25], s[6:7], 0, v[24:25]
	v_lshlrev_b64 v[26:27], 12, v[42:43]
	v_lshl_add_u64 v[32:33], v[24:25], 0, s[14:15]
	v_lshl_add_u64 v[24:25], v[32:33], 0, v[4:5]
	v_lshl_add_u64 v[26:27], s[8:9], 0, v[26:27]
	v_lshl_add_u64 v[36:37], v[26:27], 0, v[4:5]
	global_load_dwordx4 v[24:27], v[24:25], off
	s_nop 0
	global_load_dwordx4 v[28:31], v[36:37], off
	v_lshl_add_u64 v[32:33], v[32:33], 0, v[6:7]
	global_load_dwordx4 v[32:35], v[32:33], off
	s_nop 0
	global_load_dwordx4 v[36:39], v[36:37], off offset:256
	s_waitcnt vmcnt(6)
	v_lshlrev_b32_e32 v48, 16, v12
	v_lshlrev_b32_e32 v44, 16, v20
	v_and_b32_e32 v45, 0xffff0000, v20
	v_lshlrev_b32_e32 v20, 16, v21
	v_and_b32_e32 v21, 0xffff0000, v21
	v_and_b32_e32 v49, 0xffff0000, v12
	v_lshlrev_b32_e32 v12, 16, v13
	v_and_b32_e32 v13, 0xffff0000, v13
	v_pk_mul_f32 v[52:53], v[156:157], s[16:17] op_sel_hi:[1,0]
	v_pk_mul_f32 v[54:55], v[154:155], s[16:17] op_sel_hi:[1,0]
	v_lshlrev_b32_e32 v46, 16, v22
	v_and_b32_e32 v47, 0xffff0000, v22
	v_lshlrev_b32_e32 v50, 16, v14
	v_and_b32_e32 v51, 0xffff0000, v14
	v_pk_fma_f32 v[12:13], v[52:53], v[20:21], v[12:13]
	v_pk_fma_f32 v[20:21], v[54:55], v[44:45], v[48:49]
	v_pk_mul_f32 v[44:45], v[146:147], s[16:17] op_sel_hi:[1,0]
	v_lshlrev_b32_e32 v22, 16, v23
	v_pk_fma_f32 v[44:45], v[44:45], v[46:47], v[50:51]
	v_mov_b32_e32 v47, v199
	v_mov_b32_e32 v46, v199
	v_cvt_pk_fp8_f32 v47, v44, v45
	v_cvt_pk_fp8_f32 v46, v20, v21
	v_and_b32_e32 v23, 0xffff0000, v23
	v_lshlrev_b32_e32 v14, 16, v15
	v_and_b32_e32 v15, 0xffff0000, v15
	v_pk_mul_f32 v[20:21], v[148:149], s[16:17] op_sel_hi:[1,0]
	v_pk_mul_f32 v[44:45], v[160:161], s[16:17] op_sel_hi:[1,0]
	v_pk_fma_f32 v[14:15], v[20:21], v[22:23], v[14:15]
	v_lshlrev_b32_e32 v20, 16, v8
	v_cvt_pk_fp8_f32 v47, v14, v15 op_sel:[0,0,1]
	v_lshlrev_b32_e32 v14, 16, v17
	v_and_b32_e32 v15, 0xffff0000, v17
	v_and_b32_e32 v21, 0xffff0000, v8
	v_lshlrev_b32_e32 v8, 16, v9
	v_and_b32_e32 v9, 0xffff0000, v9
	v_cvt_pk_fp8_f32 v46, v12, v13 op_sel:[0,0,1]
	v_lshlrev_b32_e32 v12, 16, v16
	v_and_b32_e32 v13, 0xffff0000, v16
	v_lshlrev_b32_e32 v16, 16, v18
	v_and_b32_e32 v17, 0xffff0000, v18
	v_lshlrev_b32_e32 v22, 16, v10
	v_and_b32_e32 v23, 0xffff0000, v10
	v_pk_mul_f32 v[48:49], v[158:159], s[16:17] op_sel_hi:[1,0]
	v_pk_fma_f32 v[8:9], v[44:45], v[14:15], v[8:9]
	v_pk_mul_f32 v[14:15], v[150:151], s[16:17] op_sel_hi:[1,0]
	v_pk_fma_f32 v[12:13], v[48:49], v[12:13], v[20:21]
	v_pk_fma_f32 v[14:15], v[14:15], v[16:17], v[22:23]
	v_mov_b32_e32 v16, v199
	v_mov_b32_e32 v17, v199
	v_cvt_pk_fp8_f32 v16, v12, v13
	v_cvt_pk_fp8_f32 v17, v14, v15
	v_lshlrev_b32_e32 v18, 16, v19
	v_and_b32_e32 v19, 0xffff0000, v19
	v_lshlrev_b32_e32 v10, 16, v11
	v_and_b32_e32 v11, 0xffff0000, v11
	v_pk_mul_f32 v[12:13], v[152:153], s[16:17] op_sel_hi:[1,0]
	v_lshlrev_b64 v[40:41], 11, v[40:41]
	v_pk_fma_f32 v[10:11], v[12:13], v[18:19], v[10:11]
	v_cvt_pk_fp8_f32 v16, v8, v9 op_sel:[0,0,1]
	v_cvt_pk_fp8_f32 v17, v10, v11 op_sel:[0,0,1]
	v_lshl_add_u64 v[8:9], s[10:11], 0, v[40:41]
	v_add_u32_e32 v40, s24, v220
	v_lshl_add_u64 v[8:9], v[8:9], 0, v[2:3]
	v_ashrrev_i32_e32 v41, 31, v40
	global_store_dwordx2 v[8:9], v[46:47], off
	global_store_dwordx2 v[8:9], v[16:17], off offset:128
	v_lshlrev_b64 v[8:9], 12, v[40:41]
	v_lshl_add_u64 v[8:9], s[8:9], 0, v[8:9]
	v_lshl_add_u64 v[12:13], v[8:9], 0, v[4:5]
	v_lshlrev_b64 v[8:9], 14, v[40:41]
	v_lshl_add_u64 v[8:9], s[6:7], 0, v[8:9]
	v_lshl_add_u64 v[16:17], v[8:9], 0, s[14:15]
	v_lshl_add_u64 v[18:19], v[16:17], 0, v[6:7]
	v_lshl_add_u64 v[20:21], v[16:17], 0, v[4:5]
	global_load_dwordx4 v[8:11], v[12:13], off offset:256
	s_nop 0
	global_load_dwordx4 v[12:15], v[12:13], off
	s_nop 0
	global_load_dwordx4 v[16:19], v[18:19], off
	s_nop 0
	global_load_dwordx4 v[20:23], v[20:21], off
	s_waitcnt vmcnt(6)
; __device__ __forceinline__ u32x4 pack8(const f32x4 a, const f32x4 b) { u32x4 w; w.x = cvtpk(a[0], a[1]); w.y = cvtpk(a[2], a[3]); w.z = cvtpk(b[0], b[1]); w.w = cvtpk(b[2], b[3]); return w; }
; __device__ __forceinline__ void unpack8(const u32x4 w, f32x4& a, f32x4& b) { a = (f32x4){bflo(w.x), bfhi(w.x), bflo(w.y), bfhi(w.y)}; b = (f32x4){bflo(w.z), bfhi(w.z), bflo(w.w), bfhi(w.w)}; }
;     __device__ __forceinline__ void load(Regs& r, const pg::Unit& u, int g, int wr, int wc, int fr, int fq) const {
;         EPI_G(g)
; #pragma unroll
;         for (int bj = 0; bj < 2; ++bj) { const int col = u.pn * 256 + bj * 128 + wc * 32 + 8 * fq; r.p[bj] = *(const u32x4*)(P + (size_t)row * NINP + PC_LA + col); r.q[bj] = *(const u32x4*)(M1 + (size_t)row * DM + col); }
;     }
;     __device__ __forceinline__ void finish(const Regs& r, const pg::Acc& acc, const pg::Unit& u, int g, int wr, int wc, int fr, int fq) const {
;         EPI_G(g)
; #pragma unroll
;         for (int bj = 0; bj < 2; ++bj) { const int col = u.pn * 256 + bj * 128 + wc * 32 + 8 * fq; f32x4 g0, g1, a0, a1; unpack8(r.p[bj], g0, g1); unpack8(r.q[bj], a0, a1);
;             const f32x4 m0 = acc[ai][bj][m][0] * isc * g0 + a0, m1v = acc[ai][bj][m][1] * isc * g1 + a1;
;             if (FP8_WOUT) *(u32x2*)(MIX8 + (size_t)row * DM + col) = pack8_fp8(m0, m1v); else *(u32x4*)(MIX + (size_t)row * DM + col) = pack8(m0, m1v); }
;     }
	v_lshlrev_b32_e32 v44, 16, v24
	v_and_b32_e32 v45, 0xffff0000, v24
	v_lshlrev_b32_e32 v24, 16, v25
	v_and_b32_e32 v25, 0xffff0000, v25
	v_lshlrev_b32_e32 v48, 16, v28
	v_and_b32_e32 v49, 0xffff0000, v28
	v_lshlrev_b32_e32 v28, 16, v29
	v_and_b32_e32 v29, 0xffff0000, v29
	v_pk_mul_f32 v[52:53], v[140:141], s[16:17] op_sel_hi:[1,0]
	v_pk_mul_f32 v[54:55], v[138:139], s[16:17] op_sel_hi:[1,0]
	v_lshlrev_b32_e32 v46, 16, v26
	v_and_b32_e32 v47, 0xffff0000, v26
	v_lshlrev_b32_e32 v50, 16, v30
	v_and_b32_e32 v51, 0xffff0000, v30
	v_pk_fma_f32 v[24:25], v[52:53], v[24:25], v[28:29]
	v_pk_fma_f32 v[28:29], v[54:55], v[44:45], v[48:49]
	v_pk_mul_f32 v[44:45], v[130:131], s[16:17] op_sel_hi:[1,0]
	v_lshlrev_b32_e32 v26, 16, v27
	v_pk_fma_f32 v[44:45], v[44:45], v[46:47], v[50:51]
	v_mov_b32_e32 v46, v199
	v_mov_b32_e32 v47, v199
	v_cvt_pk_fp8_f32 v46, v28, v29
	v_cvt_pk_fp8_f32 v47, v44, v45
	v_and_b32_e32 v27, 0xffff0000, v27
	v_lshlrev_b32_e32 v30, 16, v31
	v_and_b32_e32 v31, 0xffff0000, v31
	v_pk_mul_f32 v[28:29], v[132:133], s[16:17] op_sel_hi:[1,0]
	v_cvt_pk_fp8_f32 v46, v24, v25 op_sel:[0,0,1]
	v_pk_fma_f32 v[26:27], v[28:29], v[26:27], v[30:31]
	v_lshlrev_b32_e32 v24, 16, v32
	v_cvt_pk_fp8_f32 v47, v26, v27 op_sel:[0,0,1]
	v_and_b32_e32 v25, 0xffff0000, v32
	v_lshlrev_b32_e32 v26, 16, v33
	v_and_b32_e32 v27, 0xffff0000, v33
	v_lshlrev_b32_e32 v32, 16, v36
	v_and_b32_e32 v33, 0xffff0000, v36
	v_pk_mul_f32 v[48:49], v[142:143], s[16:17] op_sel_hi:[1,0]
	v_lshlrev_b32_e32 v28, 16, v34
	v_and_b32_e32 v29, 0xffff0000, v34
	v_lshlrev_b32_e32 v30, 16, v35
	v_and_b32_e32 v31, 0xffff0000, v35
	v_lshlrev_b32_e32 v34, 16, v37
	v_and_b32_e32 v35, 0xffff0000, v37
	v_lshlrev_b32_e32 v36, 16, v38
	v_and_b32_e32 v37, 0xffff0000, v38
	v_pk_fma_f32 v[24:25], v[48:49], v[24:25], v[32:33]
	v_pk_mul_f32 v[32:33], v[134:135], s[16:17] op_sel_hi:[1,0]
	v_lshlrev_b32_e32 v38, 16, v39
	v_pk_fma_f32 v[28:29], v[32:33], v[28:29], v[36:37]
	v_mov_b32_e32 v32, v199
	v_mov_b32_e32 v33, v199
	v_cvt_pk_fp8_f32 v32, v24, v25
	v_cvt_pk_fp8_f32 v33, v28, v29
	v_and_b32_e32 v39, 0xffff0000, v39
	v_pk_mul_f32 v[44:45], v[144:145], s[16:17] op_sel_hi:[1,0]
	v_pk_mul_f32 v[24:25], v[136:137], s[16:17] op_sel_hi:[1,0]
	v_pk_fma_f32 v[26:27], v[44:45], v[26:27], v[34:35]
	v_pk_fma_f32 v[24:25], v[24:25], v[30:31], v[38:39]
	v_lshlrev_b64 v[42:43], 11, v[42:43]
	v_cvt_pk_fp8_f32 v32, v26, v27 op_sel:[0,0,1]
	v_cvt_pk_fp8_f32 v33, v24, v25 op_sel:[0,0,1]
	v_lshl_add_u64 v[24:25], s[10:11], 0, v[42:43]
	v_add_u32_e32 v42, s25, v220
	v_lshl_add_u64 v[24:25], v[24:25], 0, v[2:3]
	v_ashrrev_i32_e32 v43, 31, v42
	global_store_dwordx2 v[24:25], v[46:47], off
	global_store_dwordx2 v[24:25], v[32:33], off offset:128
	v_lshlrev_b64 v[24:25], 14, v[42:43]
	v_lshl_add_u64 v[24:25], s[6:7], 0, v[24:25]
	v_lshlrev_b64 v[26:27], 12, v[42:43]
	v_lshl_add_u64 v[32:33], v[24:25], 0, s[14:15]
	v_lshl_add_u64 v[24:25], v[32:33], 0, v[4:5]
	v_lshl_add_u64 v[26:27], s[8:9], 0, v[26:27]
	v_lshl_add_u64 v[36:37], v[26:27], 0, v[4:5]
	global_load_dwordx4 v[24:27], v[24:25], off
	s_nop 0
	global_load_dwordx4 v[28:31], v[36:37], off
	v_lshl_add_u64 v[32:33], v[32:33], 0, v[6:7]
	global_load_dwordx4 v[32:35], v[32:33], off
	s_nop 0
	global_load_dwordx4 v[36:39], v[36:37], off offset:256
	s_waitcnt vmcnt(6)
	v_lshlrev_b32_e32 v48, 16, v12
	v_lshlrev_b32_e32 v44, 16, v20
	v_and_b32_e32 v45, 0xffff0000, v20
	v_lshlrev_b32_e32 v20, 16, v21
	v_and_b32_e32 v21, 0xffff0000, v21
	v_and_b32_e32 v49, 0xffff0000, v12
	v_lshlrev_b32_e32 v12, 16, v13
	v_and_b32_e32 v13, 0xffff0000, v13
	v_pk_mul_f32 v[52:53], v[124:125], s[16:17] op_sel_hi:[1,0]
	v_pk_mul_f32 v[54:55], v[122:123], s[16:17] op_sel_hi:[1,0]
	v_lshlrev_b32_e32 v46, 16, v22
	v_and_b32_e32 v47, 0xffff0000, v22
	v_lshlrev_b32_e32 v50, 16, v14
	v_and_b32_e32 v51, 0xffff0000, v14
	v_pk_fma_f32 v[12:13], v[52:53], v[20:21], v[12:13]
	v_pk_fma_f32 v[20:21], v[54:55], v[44:45], v[48:49]
	v_pk_mul_f32 v[44:45], v[114:115], s[16:17] op_sel_hi:[1,0]
	v_lshlrev_b32_e32 v22, 16, v23
	v_pk_fma_f32 v[44:45], v[44:45], v[46:47], v[50:51]
	v_mov_b32_e32 v47, v199
	v_mov_b32_e32 v46, v199
	v_cvt_pk_fp8_f32 v47, v44, v45
	v_cvt_pk_fp8_f32 v46, v20, v21
	v_and_b32_e32 v23, 0xffff0000, v23
	v_lshlrev_b32_e32 v14, 16, v15
	v_and_b32_e32 v15, 0xffff0000, v15
	v_pk_mul_f32 v[20:21], v[116:117], s[16:17] op_sel_hi:[1,0]
	v_pk_mul_f32 v[44:45], v[128:129], s[16:17] op_sel_hi:[1,0]
	v_pk_fma_f32 v[14:15], v[20:21], v[22:23], v[14:15]
	v_lshlrev_b32_e32 v20, 16, v8
	v_cvt_pk_fp8_f32 v47, v14, v15 op_sel:[0,0,1]
	v_lshlrev_b32_e32 v14, 16, v17
	v_and_b32_e32 v15, 0xffff0000, v17
	v_and_b32_e32 v21, 0xffff0000, v8
	v_lshlrev_b32_e32 v8, 16, v9
	v_and_b32_e32 v9, 0xffff0000, v9
	v_cvt_pk_fp8_f32 v46, v12, v13 op_sel:[0,0,1]
	v_lshlrev_b32_e32 v12, 16, v16
	v_and_b32_e32 v13, 0xffff0000, v16
	v_lshlrev_b32_e32 v16, 16, v18
	v_and_b32_e32 v17, 0xffff0000, v18
	v_lshlrev_b32_e32 v22, 16, v10
	v_and_b32_e32 v23, 0xffff0000, v10
	v_pk_mul_f32 v[48:49], v[126:127], s[16:17] op_sel_hi:[1,0]
	v_pk_fma_f32 v[8:9], v[44:45], v[14:15], v[8:9]
	v_pk_mul_f32 v[14:15], v[118:119], s[16:17] op_sel_hi:[1,0]
	v_pk_fma_f32 v[12:13], v[48:49], v[12:13], v[20:21]
	v_pk_fma_f32 v[14:15], v[14:15], v[16:17], v[22:23]
	v_mov_b32_e32 v16, v199
	v_mov_b32_e32 v17, v199
	v_cvt_pk_fp8_f32 v16, v12, v13
	v_cvt_pk_fp8_f32 v17, v14, v15
	v_lshlrev_b32_e32 v18, 16, v19
	v_and_b32_e32 v19, 0xffff0000, v19
	v_lshlrev_b32_e32 v10, 16, v11
	v_and_b32_e32 v11, 0xffff0000, v11
	v_pk_mul_f32 v[12:13], v[120:121], s[16:17] op_sel_hi:[1,0]
	v_lshlrev_b64 v[40:41], 11, v[40:41]
	v_pk_fma_f32 v[10:11], v[12:13], v[18:19], v[10:11]
	v_cvt_pk_fp8_f32 v16, v8, v9 op_sel:[0,0,1]
	v_cvt_pk_fp8_f32 v17, v10, v11 op_sel:[0,0,1]
	v_lshl_add_u64 v[8:9], s[10:11], 0, v[40:41]
	v_add_u32_e32 v40, s22, v220
	v_lshl_add_u64 v[8:9], v[8:9], 0, v[2:3]
	v_ashrrev_i32_e32 v41, 31, v40
	global_store_dwordx2 v[8:9], v[46:47], off
	global_store_dwordx2 v[8:9], v[16:17], off offset:128
	v_lshlrev_b64 v[8:9], 12, v[40:41]
	v_lshl_add_u64 v[8:9], s[8:9], 0, v[8:9]
	v_lshl_add_u64 v[12:13], v[8:9], 0, v[4:5]
	v_lshlrev_b64 v[8:9], 14, v[40:41]
	v_lshl_add_u64 v[8:9], s[6:7], 0, v[8:9]
	v_lshl_add_u64 v[16:17], v[8:9], 0, s[14:15]
	v_lshl_add_u64 v[44:45], v[16:17], 0, v[6:7]
	global_load_dwordx4 v[8:11], v[12:13], off offset:256
	s_nop 0
	global_load_dwordx4 v[12:15], v[12:13], off
	v_lshl_add_u64 v[46:47], v[16:17], 0, v[4:5]
	global_load_dwordx4 v[16:19], v[44:45], off
	global_load_dwordx4 v[20:23], v[46:47], off
	s_waitcnt vmcnt(6)
; __device__ __forceinline__ u32x4 pack8(const f32x4 a, const f32x4 b) { u32x4 w; w.x = cvtpk(a[0], a[1]); w.y = cvtpk(a[2], a[3]); w.z = cvtpk(b[0], b[1]); w.w = cvtpk(b[2], b[3]); return w; }
; __device__ __forceinline__ void unpack8(const u32x4 w, f32x4& a, f32x4& b) { a = (f32x4){bflo(w.x), bfhi(w.x), bflo(w.y), bfhi(w.y)}; b = (f32x4){bflo(w.z), bfhi(w.z), bflo(w.w), bfhi(w.w)}; }
;     __device__ __forceinline__ void load(Regs& r, const pg::Unit& u, int g, int wr, int wc, int fr, int fq) const {
;         EPI_G(g)
; #pragma unroll
;         for (int bj = 0; bj < 2; ++bj) { const int col = u.pn * 256 + bj * 128 + wc * 32 + 8 * fq; r.p[bj] = *(const u32x4*)(P + (size_t)row * NINP + PC_LA + col); r.q[bj] = *(const u32x4*)(M1 + (size_t)row * DM + col); }
;     }
;     __device__ __forceinline__ void finish(const Regs& r, const pg::Acc& acc, const pg::Unit& u, int g, int wr, int wc, int fr, int fq) const {
;         EPI_G(g)
; #pragma unroll
;         for (int bj = 0; bj < 2; ++bj) { const int col = u.pn * 256 + bj * 128 + wc * 32 + 8 * fq; f32x4 g0, g1, a0, a1; unpack8(r.p[bj], g0, g1); unpack8(r.q[bj], a0, a1);
;             const f32x4 m0 = acc[ai][bj][m][0] * isc * g0 + a0, m1v = acc[ai][bj][m][1] * isc * g1 + a1;
;             if (FP8_WOUT) *(u32x2*)(MIX8 + (size_t)row * DM + col) = pack8_fp8(m0, m1v); else *(u32x4*)(MIX + (size_t)row * DM + col) = pack8(m0, m1v); }
;     }
	v_lshlrev_b32_e32 v44, 16, v24
	v_and_b32_e32 v45, 0xffff0000, v24
	v_lshlrev_b32_e32 v24, 16, v25
	v_and_b32_e32 v25, 0xffff0000, v25
	v_lshlrev_b32_e32 v48, 16, v28
	v_and_b32_e32 v49, 0xffff0000, v28
	v_lshlrev_b32_e32 v28, 16, v29
	v_and_b32_e32 v29, 0xffff0000, v29
	v_pk_mul_f32 v[52:53], v[108:109], s[16:17] op_sel_hi:[1,0]
	v_pk_mul_f32 v[54:55], v[106:107], s[16:17] op_sel_hi:[1,0]
	v_lshlrev_b32_e32 v46, 16, v26
	v_and_b32_e32 v47, 0xffff0000, v26
	v_lshlrev_b32_e32 v50, 16, v30
	v_and_b32_e32 v51, 0xffff0000, v30
	v_pk_fma_f32 v[24:25], v[52:53], v[24:25], v[28:29]
	v_pk_fma_f32 v[28:29], v[54:55], v[44:45], v[48:49]
	v_pk_mul_f32 v[44:45], v[98:99], s[16:17] op_sel_hi:[1,0]
	v_lshlrev_b32_e32 v26, 16, v27
	v_pk_fma_f32 v[44:45], v[44:45], v[46:47], v[50:51]
	v_mov_b32_e32 v46, v199
	v_mov_b32_e32 v47, v199
	v_cvt_pk_fp8_f32 v46, v28, v29
	v_cvt_pk_fp8_f32 v47, v44, v45
	v_and_b32_e32 v27, 0xffff0000, v27
	v_lshlrev_b32_e32 v30, 16, v31
	v_and_b32_e32 v31, 0xffff0000, v31
	v_pk_mul_f32 v[28:29], v[100:101], s[16:17] op_sel_hi:[1,0]
	v_cvt_pk_fp8_f32 v46, v24, v25 op_sel:[0,0,1]
	v_pk_fma_f32 v[26:27], v[28:29], v[26:27], v[30:31]
	v_lshlrev_b32_e32 v24, 16, v32
	v_cvt_pk_fp8_f32 v47, v26, v27 op_sel:[0,0,1]
	v_and_b32_e32 v25, 0xffff0000, v32
	v_lshlrev_b32_e32 v26, 16, v33
	v_and_b32_e32 v27, 0xffff0000, v33
	v_lshlrev_b32_e32 v32, 16, v36
	v_and_b32_e32 v33, 0xffff0000, v36
	v_pk_mul_f32 v[48:49], v[110:111], s[16:17] op_sel_hi:[1,0]
	v_lshlrev_b32_e32 v28, 16, v34
	v_and_b32_e32 v29, 0xffff0000, v34
	v_lshlrev_b32_e32 v30, 16, v35
	v_and_b32_e32 v31, 0xffff0000, v35
	v_lshlrev_b32_e32 v34, 16, v37
	v_and_b32_e32 v35, 0xffff0000, v37
	v_lshlrev_b32_e32 v36, 16, v38
	v_and_b32_e32 v37, 0xffff0000, v38
	v_pk_fma_f32 v[24:25], v[48:49], v[24:25], v[32:33]
	v_pk_mul_f32 v[32:33], v[102:103], s[16:17] op_sel_hi:[1,0]
	v_lshlrev_b32_e32 v38, 16, v39
	v_pk_fma_f32 v[28:29], v[32:33], v[28:29], v[36:37]
	v_mov_b32_e32 v32, v199
	v_mov_b32_e32 v33, v199
	v_cvt_pk_fp8_f32 v32, v24, v25
	v_cvt_pk_fp8_f32 v33, v28, v29
	v_and_b32_e32 v39, 0xffff0000, v39
	v_pk_mul_f32 v[44:45], v[112:113], s[16:17] op_sel_hi:[1,0]
	v_pk_mul_f32 v[24:25], v[104:105], s[16:17] op_sel_hi:[1,0]
	v_pk_fma_f32 v[26:27], v[44:45], v[26:27], v[34:35]
	v_pk_fma_f32 v[24:25], v[24:25], v[30:31], v[38:39]
	v_lshlrev_b64 v[42:43], 11, v[42:43]
	v_cvt_pk_fp8_f32 v32, v26, v27 op_sel:[0,0,1]
	v_cvt_pk_fp8_f32 v33, v24, v25 op_sel:[0,0,1]
	v_lshl_add_u64 v[24:25], s[10:11], 0, v[42:43]
	v_add_u32_e32 v36, s19, v220
	v_lshl_add_u64 v[24:25], v[24:25], 0, v[2:3]
	v_ashrrev_i32_e32 v37, 31, v36
	global_store_dwordx2 v[24:25], v[46:47], off
	global_store_dwordx2 v[24:25], v[32:33], off offset:128
	v_lshlrev_b64 v[24:25], 14, v[36:37]
	v_lshl_add_u64 v[24:25], s[6:7], 0, v[24:25]
	v_lshlrev_b64 v[28:29], 12, v[36:37]
	v_lshl_add_u64 v[32:33], v[24:25], 0, s[14:15]
	v_lshl_add_u64 v[28:29], s[8:9], 0, v[28:29]
	v_lshl_add_u64 v[24:25], v[32:33], 0, v[4:5]
	v_lshl_add_u64 v[38:39], v[28:29], 0, v[4:5]
	global_load_dwordx4 v[24:27], v[24:25], off
	v_lshl_add_u64 v[42:43], v[32:33], 0, v[6:7]
	global_load_dwordx4 v[28:31], v[38:39], off
	global_load_dwordx4 v[4:7], v[42:43], off
	global_load_dwordx4 v[32:35], v[38:39], off offset:256
	v_lshlrev_b64 v[38:39], 11, v[40:41]
	s_waitcnt vmcnt(0)
; __device__ __forceinline__ u32x4 pack8(const f32x4 a, const f32x4 b) { u32x4 w; w.x = cvtpk(a[0], a[1]); w.y = cvtpk(a[2], a[3]); w.z = cvtpk(b[0], b[1]); w.w = cvtpk(b[2], b[3]); return w; }
; __device__ __forceinline__ void unpack8(const u32x4 w, f32x4& a, f32x4& b) { a = (f32x4){bflo(w.x), bfhi(w.x), bflo(w.y), bfhi(w.y)}; b = (f32x4){bflo(w.z), bfhi(w.z), bflo(w.w), bfhi(w.w)}; }
; template <class P, class MK = NoChain>
; __device__ __forceinline__ void gemm_phase(LAS unsigned char* lds, const P& p, const MK& mk = MK(), bool chain_out = false, bool chained_in = false) {
;     ...
;     if constexpr (!PEEL) {
; #pragma unroll
;         for (int a = 0; a < 2; ++a)
; #pragma unroll
;             for (int b = 0; b < 2; ++b)
; #pragma unroll
;                 for (int m = 0; m < 4; ++m)
; #pragma unroll
;                     for (int n = 0; n < 2; ++n) { typedef double d2_ __attribute__((ext_vector_type(2))); d2_ z_; asm volatile("v_mov_b64 %0, 0" : "=v"(z_.x)); asm volatile("v_mov_b64 %0, 0" : "=v"(z_.y)); acc[a][b][m][n] = __builtin_bit_cast(f32x4, z_); }
;     }
;     __device__ __forceinline__ void load(Regs& r, const pg::Unit& u, int g, int wr, int wc, int fr, int fq) const {
;         EPI_G(g)
; #pragma unroll
;         for (int bj = 0; bj < 2; ++bj) { const int col = u.pn * 256 + bj * 128 + wc * 32 + 8 * fq; r.p[bj] = *(const u32x4*)(P + (size_t)row * NINP + PC_LA + col); r.q[bj] = *(const u32x4*)(M1 + (size_t)row * DM + col); }
;     }
;     __device__ __forceinline__ void finish(const Regs& r, const pg::Acc& acc, const pg::Unit& u, int g, int wr, int wc, int fr, int fq) const {
;         EPI_G(g)
; #pragma unroll
;         for (int bj = 0; bj < 2; ++bj) { const int col = u.pn * 256 + bj * 128 + wc * 32 + 8 * fq; f32x4 g0, g1, a0, a1; unpack8(r.p[bj], g0, g1); unpack8(r.q[bj], a0, a1);
;             const f32x4 m0 = acc[ai][bj][m][0] * isc * g0 + a0, m1v = acc[ai][bj][m][1] * isc * g1 + a1;
;             if (FP8_WOUT) *(u32x2*)(MIX8 + (size_t)row * DM + col) = pack8_fp8(m0, m1v); else *(u32x4*)(MIX + (size_t)row * DM + col) = pack8(m0, m1v); }
;     }
	v_lshlrev_b32_e32 v40, 16, v20
	v_and_b32_e32 v41, 0xffff0000, v20
	v_lshlrev_b32_e32 v20, 16, v21
	v_and_b32_e32 v21, 0xffff0000, v21
	v_lshlrev_b32_e32 v44, 16, v12
	v_and_b32_e32 v45, 0xffff0000, v12
	v_lshlrev_b32_e32 v12, 16, v13
	v_and_b32_e32 v13, 0xffff0000, v13
	v_pk_mul_f32 v[48:49], v[92:93], s[16:17] op_sel_hi:[1,0]
	v_pk_mul_f32 v[50:51], v[90:91], s[16:17] op_sel_hi:[1,0]
	v_lshlrev_b32_e32 v42, 16, v22
	v_and_b32_e32 v43, 0xffff0000, v22
	v_lshlrev_b32_e32 v46, 16, v14
	v_and_b32_e32 v47, 0xffff0000, v14
	v_pk_fma_f32 v[12:13], v[48:49], v[20:21], v[12:13]
	v_pk_fma_f32 v[20:21], v[50:51], v[40:41], v[44:45]
	v_pk_mul_f32 v[40:41], v[82:83], s[16:17] op_sel_hi:[1,0]
	v_lshlrev_b32_e32 v22, 16, v23
	v_pk_fma_f32 v[40:41], v[40:41], v[42:43], v[46:47]
	v_mov_b32_e32 v43, v199
	v_mov_b32_e32 v42, v199
	v_cvt_pk_fp8_f32 v43, v40, v41
	v_cvt_pk_fp8_f32 v42, v20, v21
	v_and_b32_e32 v23, 0xffff0000, v23
	v_lshlrev_b32_e32 v14, 16, v15
	v_and_b32_e32 v15, 0xffff0000, v15
	v_pk_mul_f32 v[20:21], v[84:85], s[16:17] op_sel_hi:[1,0]
	v_pk_mul_f32 v[40:41], v[96:97], s[16:17] op_sel_hi:[1,0]
	v_pk_fma_f32 v[14:15], v[20:21], v[22:23], v[14:15]
	v_lshlrev_b32_e32 v20, 16, v8
	v_cvt_pk_fp8_f32 v43, v14, v15 op_sel:[0,0,1]
	v_lshlrev_b32_e32 v14, 16, v17
	v_and_b32_e32 v15, 0xffff0000, v17
	v_and_b32_e32 v21, 0xffff0000, v8
	v_lshlrev_b32_e32 v8, 16, v9
	v_and_b32_e32 v9, 0xffff0000, v9
	v_cvt_pk_fp8_f32 v42, v12, v13 op_sel:[0,0,1]
	v_lshlrev_b32_e32 v12, 16, v16
	v_and_b32_e32 v13, 0xffff0000, v16
	v_lshlrev_b32_e32 v16, 16, v18
	v_and_b32_e32 v17, 0xffff0000, v18
	v_lshlrev_b32_e32 v22, 16, v10
	v_and_b32_e32 v23, 0xffff0000, v10
	v_pk_fma_f32 v[8:9], v[40:41], v[14:15], v[8:9]
	v_pk_mul_f32 v[14:15], v[86:87], s[16:17] op_sel_hi:[1,0]
	v_pk_mul_f32 v[44:45], v[94:95], s[16:17] op_sel_hi:[1,0]
	v_pk_fma_f32 v[14:15], v[14:15], v[16:17], v[22:23]
	v_mov_b32_e32 v17, v199
	v_cvt_pk_fp8_f32 v17, v14, v15
	v_pk_fma_f32 v[12:13], v[44:45], v[12:13], v[20:21]
	v_mov_b32_e32 v16, v199
	v_lshlrev_b32_e32 v18, 16, v19
	v_and_b32_e32 v19, 0xffff0000, v19
	v_lshlrev_b32_e32 v10, 16, v11
	v_and_b32_e32 v11, 0xffff0000, v11
	v_cvt_pk_fp8_f32 v16, v12, v13
	v_pk_mul_f32 v[12:13], v[88:89], s[16:17] op_sel_hi:[1,0]
	v_cvt_pk_fp8_f32 v16, v8, v9 op_sel:[0,0,1]
	v_pk_fma_f32 v[10:11], v[12:13], v[18:19], v[10:11]
	v_lshl_add_u64 v[8:9], s[10:11], 0, v[38:39]
	v_cvt_pk_fp8_f32 v17, v10, v11 op_sel:[0,0,1]
	v_lshl_add_u64 v[8:9], v[8:9], 0, v[2:3]
	global_store_dwordx2 v[8:9], v[42:43], off
	global_store_dwordx2 v[8:9], v[16:17], off offset:128
	v_lshlrev_b64 v[8:9], 11, v[36:37]
	v_lshlrev_b32_e32 v10, 16, v24
	v_and_b32_e32 v11, 0xffff0000, v24
	v_lshlrev_b32_e32 v18, 16, v28
	v_and_b32_e32 v19, 0xffff0000, v28
	v_lshlrev_b32_e32 v20, 16, v29
	v_and_b32_e32 v21, 0xffff0000, v29
	v_pk_mul_f32 v[28:29], v[74:75], s[16:17] op_sel_hi:[1,0]
	v_lshlrev_b32_e32 v14, 16, v26
	v_and_b32_e32 v15, 0xffff0000, v26
	v_lshlrev_b32_e32 v22, 16, v30
	v_and_b32_e32 v23, 0xffff0000, v30
	v_pk_fma_f32 v[10:11], v[28:29], v[10:11], v[18:19]
	v_pk_mul_f32 v[18:19], v[66:67], s[16:17] op_sel_hi:[1,0]
	v_lshlrev_b32_e32 v12, 16, v25
	v_pk_fma_f32 v[14:15], v[18:19], v[14:15], v[22:23]
	v_mov_b32_e32 v19, v199
	v_mov_b32_e32 v18, v199
	v_cvt_pk_fp8_f32 v19, v14, v15
	v_cvt_pk_fp8_f32 v18, v10, v11
	v_and_b32_e32 v13, 0xffff0000, v25
	v_lshlrev_b32_e32 v16, 16, v27
	v_and_b32_e32 v17, 0xffff0000, v27
	v_lshlrev_b32_e32 v24, 16, v31
	v_and_b32_e32 v25, 0xffff0000, v31
	v_pk_mul_f32 v[10:11], v[68:69], s[16:17] op_sel_hi:[1,0]
	v_pk_mul_f32 v[26:27], v[76:77], s[16:17] op_sel_hi:[1,0]
	v_pk_fma_f32 v[10:11], v[10:11], v[16:17], v[24:25]
	v_pk_fma_f32 v[12:13], v[26:27], v[12:13], v[20:21]
	v_cvt_pk_fp8_f32 v19, v10, v11 op_sel:[0,0,1]
	v_lshlrev_b32_e32 v10, 16, v4
	v_and_b32_e32 v11, 0xffff0000, v4
	v_lshlrev_b32_e32 v14, 16, v32
	v_and_b32_e32 v15, 0xffff0000, v32
	v_pk_mul_f32 v[26:27], v[78:79], s[16:17] op_sel_hi:[1,0]
	v_cvt_pk_fp8_f32 v18, v12, v13 op_sel:[0,0,1]
	v_lshlrev_b32_e32 v12, 16, v6
	v_and_b32_e32 v13, 0xffff0000, v6
	v_lshlrev_b32_e32 v20, 16, v34
	v_and_b32_e32 v21, 0xffff0000, v34
	v_pk_fma_f32 v[10:11], v[26:27], v[10:11], v[14:15]
	v_pk_mul_f32 v[14:15], v[70:71], s[16:17] op_sel_hi:[1,0]
	v_lshlrev_b32_e32 v4, 16, v5
	v_pk_fma_f32 v[12:13], v[14:15], v[12:13], v[20:21]
	v_mov_b32_e32 v14, v199
	v_mov_b32_e32 v15, v199
	v_cvt_pk_fp8_f32 v14, v10, v11
	v_cvt_pk_fp8_f32 v15, v12, v13
	v_and_b32_e32 v5, 0xffff0000, v5
	v_lshlrev_b32_e32 v6, 16, v7
	v_and_b32_e32 v7, 0xffff0000, v7
	v_lshlrev_b32_e32 v16, 16, v33
	v_and_b32_e32 v17, 0xffff0000, v33
	v_lshlrev_b32_e32 v22, 16, v35
	v_and_b32_e32 v23, 0xffff0000, v35
	v_pk_mul_f32 v[24:25], v[80:81], s[16:17] op_sel_hi:[1,0]
	v_pk_mul_f32 v[10:11], v[72:73], s[16:17] op_sel_hi:[1,0]
	v_pk_fma_f32 v[4:5], v[24:25], v[4:5], v[16:17]
	v_pk_fma_f32 v[6:7], v[10:11], v[6:7], v[22:23]
	v_cvt_pk_fp8_f32 v14, v4, v5 op_sel:[0,0,1]
	v_cvt_pk_fp8_f32 v15, v6, v7 op_sel:[0,0,1]
	v_lshl_add_u64 v[4:5], s[10:11], 0, v[8:9]
	v_lshl_add_u64 v[2:3], v[4:5], 0, v[2:3]
	global_store_dwordx2 v[2:3], v[18:19], off
	global_store_dwordx2 v[2:3], v[14:15], off offset:128
	s_cbranch_vccnz .LBB0_1156
	s_mov_b64 s[2:3], 0
	v_mov_b64 v[186:187], 0
	v_mov_b64 v[188:189], 0
	v_mov_b64 v[182:183], 0
	v_mov_b64 v[184:185], 0
	v_mov_b64 v[170:171], 0
	v_mov_b64 v[172:173], 0
	v_mov_b64 v[162:163], 0
	v_mov_b64 v[164:165], 0
	v_mov_b64 v[154:155], 0
	v_mov_b64 v[156:157], 0
	v_mov_b64 v[146:147], 0
	v_mov_b64 v[148:149], 0
	v_mov_b64 v[138:139], 0
	v_mov_b64 v[140:141], 0
	v_mov_b64 v[130:131], 0
	v_mov_b64 v[132:133], 0
	v_mov_b64 v[190:191], 0
	v_mov_b64 v[192:193], 0
	v_mov_b64 v[178:179], 0
	v_mov_b64 v[180:181], 0
	v_mov_b64 v[174:175], 0
	v_mov_b64 v[176:177], 0
	v_mov_b64 v[166:167], 0
	v_mov_b64 v[168:169], 0
	v_mov_b64 v[158:159], 0
	v_mov_b64 v[160:161], 0
	v_mov_b64 v[150:151], 0
	v_mov_b64 v[152:153], 0
	v_mov_b64 v[142:143], 0
	v_mov_b64 v[144:145], 0
	v_mov_b64 v[134:135], 0
	v_mov_b64 v[136:137], 0
	v_mov_b64 v[122:123], 0
	v_mov_b64 v[124:125], 0
	v_mov_b64 v[114:115], 0
	v_mov_b64 v[116:117], 0
	v_mov_b64 v[106:107], 0
	v_mov_b64 v[108:109], 0
	v_mov_b64 v[98:99], 0
	v_mov_b64 v[100:101], 0
	v_mov_b64 v[90:91], 0
	v_mov_b64 v[92:93], 0
	v_mov_b64 v[82:83], 0
	v_mov_b64 v[84:85], 0
	v_mov_b64 v[74:75], 0
	v_mov_b64 v[76:77], 0
	v_mov_b64 v[66:67], 0
	v_mov_b64 v[68:69], 0
	v_mov_b64 v[126:127], 0
	v_mov_b64 v[128:129], 0
	v_mov_b64 v[118:119], 0
	v_mov_b64 v[120:121], 0
	v_mov_b64 v[110:111], 0
	v_mov_b64 v[112:113], 0
	v_mov_b64 v[102:103], 0
	v_mov_b64 v[104:105], 0
	v_mov_b64 v[94:95], 0
	v_mov_b64 v[96:97], 0
	v_mov_b64 v[86:87], 0
	v_mov_b64 v[88:89], 0
	v_mov_b64 v[78:79], 0
	v_mov_b64 v[80:81], 0
	v_mov_b64 v[70:71], 0
	v_mov_b64 v[72:73], 0
	s_branch .LBB0_1156

; #define CB_ISSUE(dst, k0) _Pragma("unroll") for (int k = 0; k < 2; ++k) { const unsigned pk_ = ASG[(size_t)t * 8 + (k0) + k]; const int e = pk_ >> 16, slot = pk_ & 0xffff; const unsigned char* p = OUT2b + ((size_t)T.ts[e] * 256 + slot) * DM + 1024 * hh; \
;             _Pragma("unroll") for (int j = 0; j < 2; ++j) dst[k][j] = *(const u32x2*)(p + 512 * j + 8 * lane); }
; __device__ __forceinline__ void combine_phase(CArgs& A, int l, const float* xin, LAS unsigned char* lds, int vcu, int G) {
;     ...
;     for (int t = vcu * NWAVES + wave; t < NT; t += G * NWAVES) {
;         const int b = t / SEQ;
;         Row x;
;         const ModPtr gt = mod_ptr(A, l, b, 5);
;     ...
; #pragma unroll
;         for (int hh = 0; hh < 2; ++hh) {
;             u32x2 rs[2], ra[2][2], rb[2][2]; float y[2][8];
;             { const unsigned char* p = OUT2b + (size_t)(MAXROWS + t) * DM + 1024 * hh;
; #pragma unroll
;               for (int j = 0; j < 2; ++j) rs[j] = *(const u32x2*)(p + 512 * j + 8 * lane); }
;             CB_ISSUE(ra, 0) CB_ISSUE(rb, 2)
;             asm volatile("" ::: "memory");
; #pragma unroll
;             for (int j = 0; j < 2; ++j) { f32x4 a, c; unpack8_fp8(rs[j], a, c); y[j][0] = a.x; y[j][1] = a.y; y[j][2] = a.z; y[j][3] = a.w; y[j][4] = c.x; y[j][5] = c.y; y[j][6] = c.z; y[j][7] = c.w; }
;             CB_ACC(ra, 0)
.LBB0_1734:
	s_ashr_i32 s8, s4, 31
	v_lshl_add_u64 v[2:3], s[0:1], 0, v[34:35]
	s_lshr_b32 s8, s8, 20
	v_add_co_u32_e32 v2, vcc, s5, v2
	s_add_i32 s8, s4, s8
	v_lshl_add_u64 v[4:5], s[0:1], 0, v[32:33]
	v_addc_co_u32_e32 v3, vcc, 0, v3, vcc
	s_ashr_i32 s8, s8, 12
	v_add_co_u32_e32 v50, vcc, s37, v4
	s_mul_hi_i32 s24, s8, 0xc000
	s_mul_i32 s8, s8, 0xc000
	v_addc_co_u32_e32 v51, vcc, 0, v5, vcc
	s_add_u32 s30, s34, s8
	v_add_co_u32_e32 v48, vcc, s38, v4
	s_addc_u32 s31, s35, s24
	v_lshl_add_u64 v[6:7], s[0:1], 0, v[30:31]
	v_addc_co_u32_e32 v49, vcc, 0, v5, vcc
	s_add_u32 s26, s30, 0xa000
	v_add_co_u32_e32 v46, vcc, s40, v6
	s_addc_u32 s27, s31, 0
	v_lshl_add_u64 v[8:9], s[0:1], 0, v[28:29]
	v_addc_co_u32_e32 v47, vcc, 0, v7, vcc
	s_add_u32 s24, s0, s6
	v_add_co_u32_e32 v44, vcc, s41, v8
	s_addc_u32 s25, s1, s7
	v_lshl_add_u64 v[12:13], v[4:5], 0, s[10:11]
	v_lshl_add_u64 v[74:75], v[4:5], 0, s[12:13]
	v_lshl_add_u64 v[54:55], v[4:5], 0, s[14:15]
	v_lshl_add_u64 v[52:53], v[4:5], 0, s[16:17]
	v_addc_co_u32_e32 v45, vcc, 0, v9, vcc
	global_load_dwordx2 v[8:9], v[2:3], off
	global_load_dwordx2 v[10:11], v[2:3], off offset:512
	global_load_dwordx4 v[4:7], v1, s[24:25]
	v_mov_b32_e32 v36, 0
	v_mov_b32_e32 v37, 0
	v_mov_b32_e32 v38, 0
	v_mov_b32_e32 v39, 0
	v_mov_b32_e32 v40, 0
	v_mov_b32_e32 v41, 0
	v_mov_b32_e32 v42, 0
	v_mov_b32_e32 v43, 0
	v_lshl_add_u64 v[28:29], v[28:29], 0, s[18:19]
	v_lshl_add_u64 v[30:31], v[30:31], 0, s[20:21]
	v_lshl_add_u64 v[32:33], v[32:33], 0, s[22:23]
	v_lshl_add_u64 v[34:35], v[34:35], 0, s[18:19]
	s_waitcnt vmcnt(2)
	v_cvt_pk_f32_fp8_e32 v[14:15], v8
	v_cvt_pk_f32_fp8_sdwa v[16:17], v8 src0_sel:WORD_1
	s_waitcnt vmcnt(0)
	v_readfirstlane_b32 s33, v4
	v_readfirstlane_b32 s8, v7
	v_readfirstlane_b32 s28, v6
	v_readfirstlane_b32 s29, v5
	s_bfe_u32 s42, s33, 0x100010
	s_lshl_b32 s33, s33, 11
	s_bfe_u32 s43, s29, 0x100010
	s_bfe_u32 s44, s28, 0x100010
	s_bfe_u32 s45, s8, 0x100010
	s_lshl_b32 s42, s42, 2
	s_lshl_b32 s46, s8, 11
	s_and_b32 s8, s33, 0x7fff800
	s_lshl_b32 s33, s43, 2
	s_lshl_b32 s43, s44, 2
	s_lshl_b32 s44, s45, 2
	s_add_i32 s42, s36, s42
	s_add_i32 s33, s36, s33
	s_add_i32 s43, s36, s43
	s_add_i32 s44, s36, s44
	v_mov_b32_e32 v4, s42
	v_mov_b32_e32 v5, s33
	v_mov_b32_e32 v7, s43
	v_mov_b32_e32 v71, s44
	ds_read_b32 v4, v4
	ds_read_b32 v6, v5
	ds_read_b32 v70, v7
	ds_read_b32 v72, v71
	s_lshl_b32 s29, s29, 11
	s_waitcnt lgkmcnt(3)
	v_ashrrev_i32_e32 v5, 31, v4
	s_waitcnt lgkmcnt(2)
	v_ashrrev_i32_e32 v7, 31, v6
	v_lshlrev_b64 v[4:5], 19, v[4:5]
	s_waitcnt lgkmcnt(1)
	v_ashrrev_i32_e32 v71, 31, v70
	v_lshlrev_b64 v[6:7], 19, v[6:7]
	v_lshl_add_u64 v[4:5], s[2:3], 0, v[4:5]
	s_lshl_b32 s28, s28, 11
	s_waitcnt lgkmcnt(0)
	v_ashrrev_i32_e32 v73, 31, v72
	v_lshlrev_b64 v[70:71], 19, v[70:71]
	v_lshl_add_u64 v[6:7], s[2:3], 0, v[6:7]
	v_lshl_add_u64 v[4:5], v[4:5], 0, s[8:9]
	s_and_b32 s8, s29, 0x7fff800
	v_lshlrev_b64 v[72:73], 19, v[72:73]
	v_lshl_add_u64 v[70:71], s[2:3], 0, v[70:71]
	v_lshl_add_u64 v[6:7], v[6:7], 0, s[8:9]
	s_and_b32 s8, s28, 0x7fff800
	v_lshl_add_u64 v[72:73], s[2:3], 0, v[72:73]
	v_lshl_add_u64 v[4:5], v[4:5], 0, v[18:19]
	v_lshl_add_u64 v[6:7], v[6:7], 0, v[18:19]
	v_lshl_add_u64 v[70:71], v[70:71], 0, s[8:9]
	s_and_b32 s8, s46, 0x7fff800
	global_load_dwordx2 v[76:77], v[4:5], off
	s_nop 0
	global_load_dwordx2 v[4:5], v[4:5], off offset:512
	s_nop 0
	global_load_dwordx2 v[78:79], v[6:7], off
	global_load_dwordx2 v[80:81], v[6:7], off offset:512
	v_lshl_add_u64 v[6:7], v[70:71], 0, v[18:19]
	v_lshl_add_u64 v[70:71], v[72:73], 0, s[8:9]
	global_load_dwordx2 v[72:73], v[6:7], off
	global_load_dwordx2 v[82:83], v[6:7], off offset:512
	v_lshl_add_u64 v[6:7], v[70:71], 0, v[18:19]
	global_load_dwordx2 v[70:71], v[6:7], off
	global_load_dwordx2 v[84:85], v[6:7], off offset:512
	global_load_dwordx2 v[6:7], v56, s[24:25]
	global_load_dwordx2 v[86:87], v1, s[24:25] offset:16
	v_cvt_pk_f32_fp8_e32 v[62:63], v9
	v_cvt_pk_f32_fp8_sdwa v[8:9], v9 src0_sel:WORD_1
	v_cvt_pk_f32_fp8_e32 v[64:65], v10
	v_cvt_pk_f32_fp8_sdwa v[66:67], v10 src0_sel:WORD_1
	v_cvt_pk_f32_fp8_e32 v[68:69], v11
	v_cvt_pk_f32_fp8_sdwa v[10:11], v11 src0_sel:WORD_1
	s_waitcnt vmcnt(9)
	v_cvt_pk_f32_fp8_e32 v[88:89], v76
	v_cvt_pk_f32_fp8_sdwa v[90:91], v76 src0_sel:WORD_1
	v_cvt_pk_f32_fp8_e32 v[92:93], v77
	v_cvt_pk_f32_fp8_sdwa v[76:77], v77 src0_sel:WORD_1
	s_waitcnt vmcnt(8)
	v_cvt_pk_f32_fp8_e32 v[94:95], v4
	v_cvt_pk_f32_fp8_sdwa v[96:97], v4 src0_sel:WORD_1
	v_cvt_pk_f32_fp8_e32 v[98:99], v5
	v_cvt_pk_f32_fp8_sdwa v[4:5], v5 src0_sel:WORD_1
	s_waitcnt vmcnt(7)
	v_cvt_pk_f32_fp8_e32 v[100:101], v78
	v_cvt_pk_f32_fp8_sdwa v[102:103], v78 src0_sel:WORD_1
	v_cvt_pk_f32_fp8_e32 v[104:105], v79
	v_cvt_pk_f32_fp8_sdwa v[78:79], v79 src0_sel:WORD_1
	s_waitcnt vmcnt(6)
	v_cvt_pk_f32_fp8_e32 v[106:107], v80
	v_cvt_pk_f32_fp8_sdwa v[108:109], v80 src0_sel:WORD_1
	v_cvt_pk_f32_fp8_e32 v[110:111], v81
	v_cvt_pk_f32_fp8_sdwa v[80:81], v81 src0_sel:WORD_1
	s_waitcnt vmcnt(0)
; #define CB_ISSUE(dst, k0) _Pragma("unroll") for (int k = 0; k < 2; ++k) { const unsigned pk_ = ASG[(size_t)t * 8 + (k0) + k]; const int e = pk_ >> 16, slot = pk_ & 0xffff; const unsigned char* p = OUT2b + ((size_t)T.ts[e] * 256 + slot) * DM + 1024 * hh; \
;             _Pragma("unroll") for (int j = 0; j < 2; ++j) dst[k][j] = *(const u32x2*)(p + 512 * j + 8 * lane); }
; __device__ __forceinline__ void combine_phase(CArgs& A, int l, const float* xin, LAS unsigned char* lds, int vcu, int G) {
;     ...
; #pragma unroll
;         for (int hh = 0; hh < 2; ++hh) {
;             u32x2 rs[2], ra[2][2], rb[2][2]; float y[2][8];
;             { const unsigned char* p = OUT2b + (size_t)(MAXROWS + t) * DM + 1024 * hh;
; #pragma unroll
;               for (int j = 0; j < 2; ++j) rs[j] = *(const u32x2*)(p + 512 * j + 8 * lane); }
;             CB_ISSUE(ra, 0) CB_ISSUE(rb, 2)
;             asm volatile("" ::: "memory");
; #pragma unroll
;             for (int j = 0; j < 2; ++j) { f32x4 a, c; unpack8_fp8(rs[j], a, c); y[j][0] = a.x; y[j][1] = a.y; y[j][2] = a.z; y[j][3] = a.w; y[j][4] = c.x; y[j][5] = c.y; y[j][6] = c.z; y[j][7] = c.w; }
;             CB_ACC(ra, 0)
;             asm volatile("" ::: "memory");
;             CB_ISSUE(ra, 4)
;             asm volatile("" ::: "memory");
;             CB_ACC(rb, 2)
;             asm volatile("" ::: "memory");
;             CB_ISSUE(rb, 6)
;             asm volatile("" ::: "memory");
;             CB_ACC(ra, 4)
;             asm volatile("" ::: "memory");
;             f32x4 xv[2][2], gv[2][2];
; #pragma unroll
;             for (int j = 0; j < 2; ++j)
; #pragma unroll
;                 for (int q4 = 0; q4 < 2; ++q4) { const int c = 1024 * hh + 512 * j + 8 * lane + 4 * q4; xv[j][q4] = *(const f32x4*)(xin + (size_t)t * DM + c); gv[j][q4] = *(const f32x4*)(gt.acc + c); }
;             asm volatile("" ::: "memory");
;             CB_ACC(rb, 6)
	v_readfirstlane_b32 s8, v86
	v_readfirstlane_b32 s28, v87
	s_bfe_u32 s29, s8, 0x100010
	s_bfe_u32 s33, s28, 0x100010
	s_lshl_b32 s29, s29, 2
	v_pk_fma_f32 v[14:15], v[6:7], v[88:89], v[14:15] op_sel_hi:[0,1,1]
	v_pk_fma_f32 v[16:17], v[6:7], v[90:91], v[16:17] op_sel_hi:[0,1,1]
	v_pk_fma_f32 v[62:63], v[6:7], v[92:93], v[62:63] op_sel_hi:[0,1,1]
	v_pk_fma_f32 v[8:9], v[6:7], v[76:77], v[8:9] op_sel_hi:[0,1,1]
	v_pk_fma_f32 v[64:65], v[6:7], v[94:95], v[64:65] op_sel_hi:[0,1,1]
	v_pk_fma_f32 v[66:67], v[6:7], v[96:97], v[66:67] op_sel_hi:[0,1,1]
	v_pk_fma_f32 v[68:69], v[6:7], v[98:99], v[68:69] op_sel_hi:[0,1,1]
	v_pk_fma_f32 v[4:5], v[6:7], v[4:5], v[10:11] op_sel_hi:[0,1,1]
	s_lshl_b32 s33, s33, 2
	s_add_i32 s29, s36, s29
	v_pk_fma_f32 v[10:11], v[6:7], v[100:101], v[14:15] op_sel:[1,0,0]
	v_pk_fma_f32 v[14:15], v[6:7], v[102:103], v[16:17] op_sel:[1,0,0]
	v_pk_fma_f32 v[16:17], v[6:7], v[104:105], v[62:63] op_sel:[1,0,0]
	v_pk_fma_f32 v[8:9], v[6:7], v[78:79], v[8:9] op_sel:[1,0,0]
	v_pk_fma_f32 v[62:63], v[6:7], v[106:107], v[64:65] op_sel:[1,0,0]
	v_pk_fma_f32 v[64:65], v[6:7], v[108:109], v[66:67] op_sel:[1,0,0]
	v_pk_fma_f32 v[66:67], v[6:7], v[110:111], v[68:69] op_sel:[1,0,0]
	v_pk_fma_f32 v[4:5], v[6:7], v[80:81], v[4:5] op_sel:[1,0,0]
	s_add_i32 s33, s36, s33
	v_mov_b32_e32 v6, s29
	v_mov_b32_e32 v7, s33
	ds_read_b32 v6, v6
	ds_read_b32 v68, v7
	s_lshl_b32 s8, s8, 11
	s_lshl_b32 s28, s28, 11
	s_and_b32 s8, s8, 0x7fff800
	s_waitcnt lgkmcnt(1)
	v_ashrrev_i32_e32 v7, 31, v6
	s_waitcnt lgkmcnt(0)
	v_ashrrev_i32_e32 v69, 31, v68
	v_lshlrev_b64 v[6:7], 19, v[6:7]
	v_lshlrev_b64 v[68:69], 19, v[68:69]
	v_lshl_add_u64 v[6:7], s[2:3], 0, v[6:7]
	v_lshl_add_u64 v[68:69], s[2:3], 0, v[68:69]
	v_lshl_add_u64 v[6:7], v[6:7], 0, s[8:9]
	s_and_b32 s8, s28, 0x7fff800
	v_lshl_add_u64 v[68:69], v[68:69], 0, s[8:9]
	v_lshl_add_u64 v[6:7], v[6:7], 0, v[18:19]
	v_lshl_add_u64 v[68:69], v[68:69], 0, v[18:19]
	global_load_dwordx2 v[76:77], v[6:7], off
	s_nop 0
	global_load_dwordx2 v[6:7], v[6:7], off offset:512
	s_nop 0
	global_load_dwordx2 v[78:79], v[68:69], off
	global_load_dwordx2 v[80:81], v[68:69], off offset:512
	global_load_dwordx2 v[68:69], v56, s[24:25] offset:8
	global_load_dwordx2 v[86:87], v1, s[24:25] offset:24
	v_cvt_pk_f32_fp8_e32 v[112:113], v72
	v_cvt_pk_f32_fp8_e32 v[118:119], v82
	v_cvt_pk_f32_fp8_sdwa v[120:121], v82 src0_sel:WORD_1
	v_cvt_pk_f32_fp8_e32 v[122:123], v83
	v_cvt_pk_f32_fp8_sdwa v[82:83], v83 src0_sel:WORD_1
	v_cvt_pk_f32_fp8_e32 v[124:125], v70
	v_cvt_pk_f32_fp8_e32 v[130:131], v84
	v_cvt_pk_f32_fp8_sdwa v[132:133], v84 src0_sel:WORD_1
	v_cvt_pk_f32_fp8_e32 v[134:135], v85
	v_cvt_pk_f32_fp8_sdwa v[84:85], v85 src0_sel:WORD_1
	v_cvt_pk_f32_fp8_sdwa v[114:115], v72 src0_sel:WORD_1
	v_cvt_pk_f32_fp8_e32 v[116:117], v73
	v_cvt_pk_f32_fp8_sdwa v[126:127], v70 src0_sel:WORD_1
	v_cvt_pk_f32_fp8_e32 v[128:129], v71
	v_cvt_pk_f32_fp8_sdwa v[72:73], v73 src0_sel:WORD_1
	v_cvt_pk_f32_fp8_sdwa v[70:71], v71 src0_sel:WORD_1
	s_waitcnt vmcnt(5)
	v_cvt_pk_f32_fp8_e32 v[88:89], v76
	s_waitcnt vmcnt(4)
	v_cvt_pk_f32_fp8_e32 v[96:97], v6
	v_cvt_pk_f32_fp8_sdwa v[98:99], v6 src0_sel:WORD_1
	v_cvt_pk_f32_fp8_e32 v[100:101], v7
	v_cvt_pk_f32_fp8_sdwa v[102:103], v7 src0_sel:WORD_1
	s_waitcnt vmcnt(1)
	v_pk_fma_f32 v[6:7], v[68:69], v[112:113], v[10:11] op_sel_hi:[0,1,1]
	s_waitcnt vmcnt(0)
	v_readfirstlane_b32 s8, v86
	v_readfirstlane_b32 s28, v87
	s_bfe_u32 s29, s8, 0x100010
	s_bfe_u32 s33, s28, 0x100010
	s_lshl_b32 s29, s29, 2
	v_pk_fma_f32 v[4:5], v[68:69], v[82:83], v[4:5] op_sel_hi:[0,1,1]
	s_lshl_b32 s33, s33, 2
	s_add_i32 s29, s36, s29
	v_pk_fma_f32 v[86:87], v[68:69], v[124:125], v[6:7] op_sel:[1,0,0]
	v_pk_fma_f32 v[124:125], v[68:69], v[84:85], v[4:5] op_sel:[1,0,0]
	s_add_i32 s33, s36, s33
	v_mov_b32_e32 v4, s29
	v_mov_b32_e32 v5, s33
	ds_read_b32 v4, v4
	ds_read_b32 v6, v5
	s_lshl_b32 s8, s8, 11
	s_lshl_b32 s28, s28, 11
	s_and_b32 s8, s8, 0x7fff800
	s_waitcnt lgkmcnt(1)
	v_ashrrev_i32_e32 v5, 31, v4
	s_waitcnt lgkmcnt(0)
	v_ashrrev_i32_e32 v7, 31, v6
	v_lshlrev_b64 v[4:5], 19, v[4:5]
	v_lshlrev_b64 v[6:7], 19, v[6:7]
	v_lshl_add_u64 v[4:5], s[2:3], 0, v[4:5]
	v_lshl_add_u64 v[6:7], s[2:3], 0, v[6:7]
	v_lshl_add_u64 v[4:5], v[4:5], 0, s[8:9]
	s_and_b32 s8, s28, 0x7fff800
	v_pk_fma_f32 v[10:11], v[68:69], v[114:115], v[14:15] op_sel_hi:[0,1,1]
	v_pk_fma_f32 v[14:15], v[68:69], v[116:117], v[16:17] op_sel_hi:[0,1,1]
	v_lshl_add_u64 v[4:5], v[4:5], 0, v[18:19]
	v_lshl_add_u64 v[6:7], v[6:7], 0, s[8:9]
	v_pk_fma_f32 v[16:17], v[68:69], v[118:119], v[62:63] op_sel_hi:[0,1,1]
	v_pk_fma_f32 v[62:63], v[68:69], v[120:121], v[64:65] op_sel_hi:[0,1,1]
	v_pk_fma_f32 v[112:113], v[68:69], v[126:127], v[10:11] op_sel:[1,0,0]
	v_pk_fma_f32 v[114:115], v[68:69], v[128:129], v[14:15] op_sel:[1,0,0]
	global_load_dwordx2 v[126:127], v[4:5], off
	global_load_dwordx2 v[128:129], v[4:5], off offset:512
	v_lshl_add_u64 v[4:5], v[6:7], 0, v[18:19]
	v_pk_fma_f32 v[64:65], v[68:69], v[122:123], v[66:67] op_sel_hi:[0,1,1]
	v_pk_fma_f32 v[118:119], v[68:69], v[130:131], v[16:17] op_sel:[1,0,0]
	v_pk_fma_f32 v[120:121], v[68:69], v[132:133], v[62:63] op_sel:[1,0,0]
	global_load_dwordx2 v[130:131], v[4:5], off
	global_load_dwordx2 v[132:133], v[4:5], off offset:512
	v_pk_fma_f32 v[8:9], v[68:69], v[72:73], v[8:9] op_sel_hi:[0,1,1]
	v_pk_fma_f32 v[122:123], v[68:69], v[134:135], v[64:65] op_sel:[1,0,0]
	global_load_dwordx2 v[134:135], v56, s[24:25] offset:16
	v_cvt_pk_f32_fp8_sdwa v[90:91], v76 src0_sel:WORD_1
	v_cvt_pk_f32_fp8_e32 v[92:93], v77
	v_cvt_pk_f32_fp8_sdwa v[94:95], v77 src0_sel:WORD_1
	v_cvt_pk_f32_fp8_e32 v[104:105], v78
	v_cvt_pk_f32_fp8_sdwa v[106:107], v78 src0_sel:WORD_1
	v_cvt_pk_f32_fp8_e32 v[108:109], v79
	v_cvt_pk_f32_fp8_sdwa v[110:111], v79 src0_sel:WORD_1
	v_cvt_pk_f32_fp8_e32 v[136:137], v80
	v_cvt_pk_f32_fp8_sdwa v[138:139], v80 src0_sel:WORD_1
	v_cvt_pk_f32_fp8_e32 v[140:141], v81
	v_cvt_pk_f32_fp8_sdwa v[142:143], v81 src0_sel:WORD_1
	v_pk_fma_f32 v[116:117], v[68:69], v[70:71], v[8:9] op_sel:[1,0,0]
	global_load_dwordx4 v[4:7], v57, s[26:27] offset:16
	global_load_dwordx4 v[8:11], v57, s[26:27]
	global_load_dwordx4 v[62:65], v[12:13], off offset:16
	global_load_dwordx4 v[66:69], v[50:51], off offset:2048
	global_load_dwordx4 v[14:17], v[48:49], off offset:-4096
	global_load_dwordx4 v[70:73], v58, s[26:27] offset:16
	s_nop 0
	global_load_dwordx4 v[74:77], v[74:75], off offset:16
	s_nop 0
	global_load_dwordx4 v[78:81], v58, s[26:27]
	global_load_dwordx2 v[12:13], v56, s[24:25] offset:24
	global_load_dwordx4 v[82:85], v1, s[24:25]
	global_load_dwordx2 v[144:145], v[2:3], off offset:1024
	s_nop 0
	global_load_dwordx2 v[2:3], v[2:3], off offset:1536
	s_waitcnt vmcnt(16)
; #define CB_ISSUE(dst, k0) _Pragma("unroll") for (int k = 0; k < 2; ++k) { const unsigned pk_ = ASG[(size_t)t * 8 + (k0) + k]; const int e = pk_ >> 16, slot = pk_ & 0xffff; const unsigned char* p = OUT2b + ((size_t)T.ts[e] * 256 + slot) * DM + 1024 * hh; \
;             _Pragma("unroll") for (int j = 0; j < 2; ++j) dst[k][j] = *(const u32x2*)(p + 512 * j + 8 * lane); }
; __device__ __forceinline__ void combine_phase(CArgs& A, int l, const float* xin, LAS unsigned char* lds, int vcu, int G) {
;     ...
;             CB_ACC(ra, 0)
;             asm volatile("" ::: "memory");
;             CB_ISSUE(ra, 4)
;             asm volatile("" ::: "memory");
;             CB_ACC(rb, 2)
;             asm volatile("" ::: "memory");
;             CB_ISSUE(rb, 6)
;             asm volatile("" ::: "memory");
;             CB_ACC(ra, 4)
;             asm volatile("" ::: "memory");
;             f32x4 xv[2][2], gv[2][2];
; #pragma unroll
;             for (int j = 0; j < 2; ++j)
; #pragma unroll
;                 for (int q4 = 0; q4 < 2; ++q4) { const int c = 1024 * hh + 512 * j + 8 * lane + 4 * q4; xv[j][q4] = *(const f32x4*)(xin + (size_t)t * DM + c); gv[j][q4] = *(const f32x4*)(gt.acc + c); }
;             asm volatile("" ::: "memory");
;             CB_ACC(rb, 6)
; #pragma unroll
;             for (int j = 0; j < 2; ++j)
; #pragma unroll
;                 for (int q4 = 0; q4 < 2; ++q4)
; #pragma unroll
;                     for (int q = 0; q < 4; ++q) x.v[2 * hh + j][4 * q4 + q] = xv[j][q4][q] + gv[j][q4][q] * y[j][4 * q4 + q];
	v_cvt_pk_f32_fp8_e32 v[146:147], v126
	v_cvt_pk_f32_fp8_sdwa v[148:149], v126 src0_sel:WORD_1
	v_cvt_pk_f32_fp8_e32 v[150:151], v127
	v_cvt_pk_f32_fp8_sdwa v[126:127], v127 src0_sel:WORD_1
	s_waitcnt vmcnt(15)
	v_cvt_pk_f32_fp8_e32 v[152:153], v128
	s_waitcnt vmcnt(14)
	v_cvt_pk_f32_fp8_e32 v[158:159], v130
	v_cvt_pk_f32_fp8_sdwa v[160:161], v130 src0_sel:WORD_1
	v_cvt_pk_f32_fp8_e32 v[162:163], v131
	v_cvt_pk_f32_fp8_sdwa v[154:155], v128 src0_sel:WORD_1
	v_cvt_pk_f32_fp8_e32 v[156:157], v129
	s_waitcnt vmcnt(12)
	v_pk_fma_f32 v[86:87], v[134:135], v[88:89], v[86:87] op_sel_hi:[0,1,1]
	v_cvt_pk_f32_fp8_sdwa v[128:129], v129 src0_sel:WORD_1
	v_cvt_pk_f32_fp8_sdwa v[130:131], v131 src0_sel:WORD_1
	v_pk_fma_f32 v[88:89], v[134:135], v[90:91], v[112:113] op_sel_hi:[0,1,1]
	v_pk_fma_f32 v[90:91], v[134:135], v[92:93], v[114:115] op_sel_hi:[0,1,1]
	v_pk_fma_f32 v[86:87], v[134:135], v[104:105], v[86:87] op_sel:[1,0,0]
	v_cvt_pk_f32_fp8_e32 v[164:165], v132
	v_cvt_pk_f32_fp8_sdwa v[166:167], v132 src0_sel:WORD_1
	v_cvt_pk_f32_fp8_e32 v[168:169], v133
	v_cvt_pk_f32_fp8_sdwa v[132:133], v133 src0_sel:WORD_1
	v_pk_fma_f32 v[92:93], v[134:135], v[94:95], v[116:117] op_sel_hi:[0,1,1]
	v_pk_fma_f32 v[88:89], v[134:135], v[106:107], v[88:89] op_sel:[1,0,0]
	v_pk_fma_f32 v[90:91], v[134:135], v[108:109], v[90:91] op_sel:[1,0,0]
	v_pk_fma_f32 v[94:95], v[134:135], v[96:97], v[118:119] op_sel_hi:[0,1,1]
	v_pk_fma_f32 v[96:97], v[134:135], v[98:99], v[120:121] op_sel_hi:[0,1,1]
	v_pk_fma_f32 v[98:99], v[134:135], v[100:101], v[122:123] op_sel_hi:[0,1,1]
	s_waitcnt vmcnt(3)
	v_pk_fma_f32 v[86:87], v[12:13], v[146:147], v[86:87] op_sel_hi:[0,1,1]
	v_pk_fma_f32 v[100:101], v[134:135], v[102:103], v[124:125] op_sel_hi:[0,1,1]
	v_pk_fma_f32 v[92:93], v[134:135], v[110:111], v[92:93] op_sel:[1,0,0]
	v_pk_fma_f32 v[88:89], v[12:13], v[148:149], v[88:89] op_sel_hi:[0,1,1]
	v_pk_fma_f32 v[90:91], v[12:13], v[150:151], v[90:91] op_sel_hi:[0,1,1]
	v_pk_fma_f32 v[86:87], v[12:13], v[158:159], v[86:87] op_sel:[1,0,0]
	s_waitcnt vmcnt(2)
	v_readfirstlane_b32 s8, v85
	v_readfirstlane_b32 s28, v84
	v_readfirstlane_b32 s29, v83
	v_readfirstlane_b32 s33, v82
	v_pk_fma_f32 v[94:95], v[134:135], v[136:137], v[94:95] op_sel:[1,0,0]
	v_pk_fma_f32 v[96:97], v[134:135], v[138:139], v[96:97] op_sel:[1,0,0]
	v_pk_fma_f32 v[98:99], v[134:135], v[140:141], v[98:99] op_sel:[1,0,0]
	v_pk_fma_f32 v[100:101], v[134:135], v[142:143], v[100:101] op_sel:[1,0,0]
	v_pk_fma_f32 v[92:93], v[12:13], v[126:127], v[92:93] op_sel_hi:[0,1,1]
	v_pk_fma_f32 v[88:89], v[12:13], v[160:161], v[88:89] op_sel:[1,0,0]
	v_pk_fma_f32 v[90:91], v[12:13], v[162:163], v[90:91] op_sel:[1,0,0]
	v_pk_fma_f32 v[14:15], v[8:9], v[86:87], v[14:15]
	s_bfe_u32 s42, s33, 0x100010
	s_lshl_b32 s33, s33, 11
	s_bfe_u32 s43, s29, 0x100010
	s_bfe_u32 s44, s28, 0x100010
	s_bfe_u32 s45, s8, 0x100010
	v_pk_fma_f32 v[94:95], v[12:13], v[152:153], v[94:95] op_sel_hi:[0,1,1]
	v_pk_fma_f32 v[96:97], v[12:13], v[154:155], v[96:97] op_sel_hi:[0,1,1]
	v_pk_fma_f32 v[98:99], v[12:13], v[156:157], v[98:99] op_sel_hi:[0,1,1]
	v_pk_fma_f32 v[100:101], v[12:13], v[128:129], v[100:101] op_sel_hi:[0,1,1]
	v_pk_fma_f32 v[92:93], v[12:13], v[130:131], v[92:93] op_sel:[1,0,0]
	v_pk_fma_f32 v[16:17], v[10:11], v[88:89], v[16:17]
	v_pk_fma_f32 v[10:11], v[4:5], v[90:91], v[62:63]
	s_lshl_b32 s46, s8, 11
	s_lshl_b32 s42, s42, 2
	s_and_b32 s8, s33, 0x7fff800
	s_lshl_b32 s33, s43, 2
	s_lshl_b32 s43, s44, 2
	s_lshl_b32 s44, s45, 2
	v_pk_mul_f32 v[62:63], v[14:15], v[14:15]
	v_pk_fma_f32 v[94:95], v[12:13], v[164:165], v[94:95] op_sel:[1,0,0]
	v_pk_fma_f32 v[96:97], v[12:13], v[166:167], v[96:97] op_sel:[1,0,0]
	v_pk_fma_f32 v[98:99], v[12:13], v[168:169], v[98:99] op_sel:[1,0,0]
	v_pk_fma_f32 v[100:101], v[12:13], v[132:133], v[100:101] op_sel:[1,0,0]
	v_pk_fma_f32 v[12:13], v[6:7], v[92:93], v[64:65]
	v_pk_mul_f32 v[64:65], v[16:17], v[16:17]
	s_add_i32 s42, s36, s42
	s_add_i32 s33, s36, s33
	s_add_i32 s44, s36, s44
	v_add_f32_e32 v62, v62, v63
	v_pk_fma_f32 v[6:7], v[78:79], v[94:95], v[66:67]
	v_pk_fma_f32 v[8:9], v[80:81], v[96:97], v[68:69]
	s_add_i32 s43, s36, s43
	v_mov_b32_e32 v63, s42
	v_mov_b32_e32 v78, s33
	v_mov_b32_e32 v80, s44
	v_add_f32_e32 v81, v62, v64
	v_pk_mul_f32 v[66:67], v[10:11], v[10:11]
	v_mov_b32_e32 v79, s43
	ds_read_b32 v62, v63
	ds_read_b32 v64, v78
	ds_read_b32 v78, v79
	ds_read_b32 v80, v80
	v_add_f32_e32 v63, v65, v81
	v_add_f32_e32 v63, v66, v63
	v_pk_mul_f32 v[68:69], v[12:13], v[12:13]
	v_add_f32_e32 v63, v67, v63
	v_add_f32_e32 v63, v68, v63
	s_waitcnt vmcnt(0)
	v_cvt_pk_f32_fp8_e32 v[106:107], v2
	v_cvt_pk_f32_fp8_sdwa v[108:109], v2 src0_sel:WORD_1
	v_cvt_pk_f32_fp8_e32 v[110:111], v3
	v_cvt_pk_f32_fp8_sdwa v[112:113], v3 src0_sel:WORD_1
	v_pk_fma_f32 v[2:3], v[70:71], v[98:99], v[74:75]
	v_pk_mul_f32 v[70:71], v[6:7], v[6:7]
	v_add_f32_e32 v66, v69, v63
	s_waitcnt lgkmcnt(3)
	v_ashrrev_i32_e32 v63, 31, v62
	s_waitcnt lgkmcnt(2)
	v_ashrrev_i32_e32 v65, 31, v64
	v_add_f32_e32 v70, v70, v66
	v_lshlrev_b64 v[62:63], 19, v[62:63]
	v_pk_fma_f32 v[4:5], v[72:73], v[100:101], v[76:77]
	s_lshl_b32 s29, s29, 11
	v_pk_mul_f32 v[72:73], v[8:9], v[8:9]
	s_waitcnt lgkmcnt(1)
	v_ashrrev_i32_e32 v79, 31, v78
	v_lshlrev_b64 v[64:65], 19, v[64:65]
	v_add_f32_e32 v70, v71, v70
	v_lshl_add_u64 v[62:63], s[2:3], 0, v[62:63]
	s_lshl_b32 s28, s28, 11
	s_waitcnt lgkmcnt(0)
; #define CB_ISSUE(dst, k0) _Pragma("unroll") for (int k = 0; k < 2; ++k) { const unsigned pk_ = ASG[(size_t)t * 8 + (k0) + k]; const int e = pk_ >> 16, slot = pk_ & 0xffff; const unsigned char* p = OUT2b + ((size_t)T.ts[e] * 256 + slot) * DM + 1024 * hh; \
;             _Pragma("unroll") for (int j = 0; j < 2; ++j) dst[k][j] = *(const u32x2*)(p + 512 * j + 8 * lane); }
; __device__ __forceinline__ void combine_phase(CArgs& A, int l, const float* xin, LAS unsigned char* lds, int vcu, int G) {
;     ...
; #pragma unroll
;         for (int hh = 0; hh < 2; ++hh) {
;             u32x2 rs[2], ra[2][2], rb[2][2]; float y[2][8];
;             { const unsigned char* p = OUT2b + (size_t)(MAXROWS + t) * DM + 1024 * hh;
; #pragma unroll
;               for (int j = 0; j < 2; ++j) rs[j] = *(const u32x2*)(p + 512 * j + 8 * lane); }
;             CB_ISSUE(ra, 0) CB_ISSUE(rb, 2)
;             asm volatile("" ::: "memory");
; #pragma unroll
;             for (int j = 0; j < 2; ++j) { f32x4 a, c; unpack8_fp8(rs[j], a, c); y[j][0] = a.x; y[j][1] = a.y; y[j][2] = a.z; y[j][3] = a.w; y[j][4] = c.x; y[j][5] = c.y; y[j][6] = c.z; y[j][7] = c.w; }
;             CB_ACC(ra, 0)
;             asm volatile("" ::: "memory");
;             CB_ISSUE(ra, 4)
;             asm volatile("" ::: "memory");
;             CB_ACC(rb, 2)
	v_ashrrev_i32_e32 v81, 31, v80
	v_lshlrev_b64 v[66:67], 19, v[78:79]
	v_lshl_add_u64 v[64:65], s[2:3], 0, v[64:65]
	v_add_f32_e32 v70, v72, v70
	v_lshl_add_u64 v[62:63], v[62:63], 0, s[8:9]
	s_and_b32 s8, s29, 0x7fff800
	v_pk_mul_f32 v[74:75], v[2:3], v[2:3]
	v_lshlrev_b64 v[68:69], 19, v[80:81]
	v_lshl_add_u64 v[66:67], s[2:3], 0, v[66:67]
	v_add_f32_e32 v70, v73, v70
	v_lshl_add_u64 v[64:65], v[64:65], 0, s[8:9]
	s_and_b32 s8, s28, 0x7fff800
	v_lshl_add_u64 v[68:69], s[2:3], 0, v[68:69]
	v_lshl_add_u64 v[62:63], v[62:63], 0, v[18:19]
	v_add_f32_e32 v72, v74, v70
	v_lshl_add_u64 v[64:65], v[64:65], 0, v[18:19]
	v_lshl_add_u64 v[66:67], v[66:67], 0, s[8:9]
	s_and_b32 s8, s46, 0x7fff800
	v_pk_mul_f32 v[76:77], v[4:5], v[4:5]
	global_load_dwordx2 v[70:71], v[62:63], off offset:1024
	s_nop 0
	global_load_dwordx2 v[62:63], v[62:63], off offset:1536
	v_add_f32_e32 v78, v75, v72
	global_load_dwordx2 v[72:73], v[64:65], off offset:1024
	global_load_dwordx2 v[74:75], v[64:65], off offset:1536
	v_lshl_add_u64 v[64:65], v[66:67], 0, v[18:19]
	v_lshl_add_u64 v[66:67], v[68:69], 0, s[8:9]
	v_add_f32_e32 v76, v76, v78
	global_load_dwordx2 v[68:69], v[64:65], off offset:1024
	global_load_dwordx2 v[78:79], v[64:65], off offset:1536
	v_lshl_add_u64 v[64:65], v[66:67], 0, v[18:19]
	v_add_f32_e32 v182, v77, v76
	global_load_dwordx2 v[66:67], v[64:65], off offset:1024
	global_load_dwordx2 v[76:77], v[64:65], off offset:1536
	global_load_dwordx2 v[64:65], v56, s[24:25]
	global_load_dwordx2 v[80:81], v1, s[24:25] offset:16
	v_cvt_pk_f32_fp8_e32 v[82:83], v144
	v_cvt_pk_f32_fp8_sdwa v[84:85], v144 src0_sel:WORD_1
	v_cvt_pk_f32_fp8_e32 v[102:103], v145
	v_cvt_pk_f32_fp8_sdwa v[104:105], v145 src0_sel:WORD_1
	s_waitcnt vmcnt(9)
	v_cvt_pk_f32_fp8_e32 v[86:87], v70
	v_cvt_pk_f32_fp8_sdwa v[88:89], v70 src0_sel:WORD_1
	v_cvt_pk_f32_fp8_e32 v[90:91], v71
	v_cvt_pk_f32_fp8_sdwa v[70:71], v71 src0_sel:WORD_1
	s_waitcnt vmcnt(8)
	v_cvt_pk_f32_fp8_e32 v[92:93], v62
	v_cvt_pk_f32_fp8_sdwa v[94:95], v62 src0_sel:WORD_1
	v_cvt_pk_f32_fp8_e32 v[96:97], v63
	v_cvt_pk_f32_fp8_sdwa v[62:63], v63 src0_sel:WORD_1
	s_waitcnt vmcnt(7)
	v_cvt_pk_f32_fp8_e32 v[98:99], v72
	v_cvt_pk_f32_fp8_sdwa v[100:101], v72 src0_sel:WORD_1
	v_cvt_pk_f32_fp8_e32 v[114:115], v73
	v_cvt_pk_f32_fp8_sdwa v[72:73], v73 src0_sel:WORD_1
	s_waitcnt vmcnt(6)
	v_cvt_pk_f32_fp8_e32 v[116:117], v74
	v_cvt_pk_f32_fp8_sdwa v[118:119], v74 src0_sel:WORD_1
	v_cvt_pk_f32_fp8_e32 v[120:121], v75
	v_cvt_pk_f32_fp8_sdwa v[74:75], v75 src0_sel:WORD_1
	s_waitcnt vmcnt(0)
	v_readfirstlane_b32 s8, v80
	v_readfirstlane_b32 s28, v81
	s_bfe_u32 s29, s8, 0x100010
	s_bfe_u32 s33, s28, 0x100010
	s_lshl_b32 s29, s29, 2
	v_pk_fma_f32 v[82:83], v[64:65], v[86:87], v[82:83] op_sel_hi:[0,1,1]
	v_pk_fma_f32 v[84:85], v[64:65], v[88:89], v[84:85] op_sel_hi:[0,1,1]
	v_pk_fma_f32 v[86:87], v[64:65], v[90:91], v[102:103] op_sel_hi:[0,1,1]
	v_pk_fma_f32 v[70:71], v[64:65], v[70:71], v[104:105] op_sel_hi:[0,1,1]
	v_pk_fma_f32 v[88:89], v[64:65], v[92:93], v[106:107] op_sel_hi:[0,1,1]
	v_pk_fma_f32 v[90:91], v[64:65], v[94:95], v[108:109] op_sel_hi:[0,1,1]
	v_pk_fma_f32 v[92:93], v[64:65], v[96:97], v[110:111] op_sel_hi:[0,1,1]
	v_pk_fma_f32 v[62:63], v[64:65], v[62:63], v[112:113] op_sel_hi:[0,1,1]
	s_lshl_b32 s33, s33, 2
	s_add_i32 s29, s36, s29
	v_pk_fma_f32 v[80:81], v[64:65], v[98:99], v[82:83] op_sel:[1,0,0]
	v_pk_fma_f32 v[82:83], v[64:65], v[100:101], v[84:85] op_sel:[1,0,0]
	v_pk_fma_f32 v[84:85], v[64:65], v[114:115], v[86:87] op_sel:[1,0,0]
	v_pk_fma_f32 v[70:71], v[64:65], v[72:73], v[70:71] op_sel:[1,0,0]
	v_pk_fma_f32 v[72:73], v[64:65], v[116:117], v[88:89] op_sel:[1,0,0]
	v_pk_fma_f32 v[86:87], v[64:65], v[118:119], v[90:91] op_sel:[1,0,0]
	v_pk_fma_f32 v[88:89], v[64:65], v[120:121], v[92:93] op_sel:[1,0,0]
	v_pk_fma_f32 v[62:63], v[64:65], v[74:75], v[62:63] op_sel:[1,0,0]
	s_add_i32 s33, s36, s33
	v_mov_b32_e32 v64, s29
	v_mov_b32_e32 v65, s33
	ds_read_b32 v64, v64
	ds_read_b32 v74, v65
	s_lshl_b32 s8, s8, 11
	s_lshl_b32 s28, s28, 11
	s_and_b32 s8, s8, 0x7fff800
	s_waitcnt lgkmcnt(1)
	v_ashrrev_i32_e32 v65, 31, v64
	s_waitcnt lgkmcnt(0)
	v_ashrrev_i32_e32 v75, 31, v74
	v_lshlrev_b64 v[64:65], 19, v[64:65]
	v_lshlrev_b64 v[74:75], 19, v[74:75]
	v_lshl_add_u64 v[64:65], s[2:3], 0, v[64:65]
	v_lshl_add_u64 v[74:75], s[2:3], 0, v[74:75]
	v_lshl_add_u64 v[64:65], v[64:65], 0, s[8:9]
	s_and_b32 s8, s28, 0x7fff800
	v_lshl_add_u64 v[74:75], v[74:75], 0, s[8:9]
	v_lshl_add_u64 v[64:65], v[64:65], 0, v[18:19]
	v_lshl_add_u64 v[74:75], v[74:75], 0, v[18:19]
	global_load_dwordx2 v[90:91], v[64:65], off offset:1024
	s_nop 0
	global_load_dwordx2 v[64:65], v[64:65], off offset:1536
	s_nop 0
	global_load_dwordx2 v[92:93], v[74:75], off offset:1024
	global_load_dwordx2 v[94:95], v[74:75], off offset:1536
	global_load_dwordx2 v[74:75], v56, s[24:25] offset:8
	global_load_dwordx2 v[96:97], v1, s[24:25] offset:24
	v_cvt_pk_f32_fp8_e32 v[122:123], v68
	v_cvt_pk_f32_fp8_e32 v[128:129], v78
	v_cvt_pk_f32_fp8_sdwa v[130:131], v78 src0_sel:WORD_1
	v_cvt_pk_f32_fp8_e32 v[132:133], v79
	v_cvt_pk_f32_fp8_sdwa v[78:79], v79 src0_sel:WORD_1
	v_cvt_pk_f32_fp8_e32 v[134:135], v66
	v_cvt_pk_f32_fp8_e32 v[140:141], v76
	v_cvt_pk_f32_fp8_sdwa v[142:143], v76 src0_sel:WORD_1
	v_cvt_pk_f32_fp8_e32 v[144:145], v77
	v_cvt_pk_f32_fp8_sdwa v[76:77], v77 src0_sel:WORD_1
	v_cvt_pk_f32_fp8_sdwa v[124:125], v68 src0_sel:WORD_1
	v_cvt_pk_f32_fp8_e32 v[126:127], v69
	v_cvt_pk_f32_fp8_sdwa v[68:69], v69 src0_sel:WORD_1
	v_cvt_pk_f32_fp8_sdwa v[136:137], v66 src0_sel:WORD_1
	v_cvt_pk_f32_fp8_e32 v[138:139], v67
	v_cvt_pk_f32_fp8_sdwa v[66:67], v67 src0_sel:WORD_1
	s_waitcnt vmcnt(5)
; #define CB_ISSUE(dst, k0) _Pragma("unroll") for (int k = 0; k < 2; ++k) { const unsigned pk_ = ASG[(size_t)t * 8 + (k0) + k]; const int e = pk_ >> 16, slot = pk_ & 0xffff; const unsigned char* p = OUT2b + ((size_t)T.ts[e] * 256 + slot) * DM + 1024 * hh; \
;             _Pragma("unroll") for (int j = 0; j < 2; ++j) dst[k][j] = *(const u32x2*)(p + 512 * j + 8 * lane); }
; __device__ __forceinline__ void row_store_f32(const Row& r, float* p, int lane) {
; #pragma unroll
;     for (int j = 0; j < 4; ++j) { *(f32x4*)(p + 512 * j + 8 * lane) = (f32x4){r.v[j][0], r.v[j][1], r.v[j][2], r.v[j][3]}; *(f32x4*)(p + 512 * j + 8 * lane + 4) = (f32x4){r.v[j][4], r.v[j][5], r.v[j][6], r.v[j][7]}; }
; }
; __device__ __forceinline__ void combine_phase(CArgs& A, int l, const float* xin, LAS unsigned char* lds, int vcu, int G) {
;     ...
;             CB_ISSUE(ra, 4)
;             asm volatile("" ::: "memory");
;             CB_ACC(rb, 2)
;             asm volatile("" ::: "memory");
;             CB_ISSUE(rb, 6)
;             asm volatile("" ::: "memory");
;             CB_ACC(ra, 4)
;             asm volatile("" ::: "memory");
;             f32x4 xv[2][2], gv[2][2];
; #pragma unroll
;             for (int j = 0; j < 2; ++j)
; #pragma unroll
;                 for (int q4 = 0; q4 < 2; ++q4) { const int c = 1024 * hh + 512 * j + 8 * lane + 4 * q4; xv[j][q4] = *(const f32x4*)(xin + (size_t)t * DM + c); gv[j][q4] = *(const f32x4*)(gt.acc + c); }
;             asm volatile("" ::: "memory");
;             CB_ACC(rb, 6)
; #pragma unroll
;             for (int j = 0; j < 2; ++j)
; #pragma unroll
;                 for (int q4 = 0; q4 < 2; ++q4)
; #pragma unroll
;                     for (int q = 0; q < 4; ++q) x.v[2 * hh + j][4 * q4 + q] = xv[j][q4][q] + gv[j][q4][q] * y[j][4 * q4 + q];
	v_cvt_pk_f32_fp8_e32 v[98:99], v90
	s_waitcnt vmcnt(4)
	v_cvt_pk_f32_fp8_e32 v[104:105], v64
	v_cvt_pk_f32_fp8_sdwa v[106:107], v64 src0_sel:WORD_1
	v_cvt_pk_f32_fp8_e32 v[108:109], v65
	v_cvt_pk_f32_fp8_sdwa v[110:111], v65 src0_sel:WORD_1
	s_waitcnt vmcnt(1)
	v_pk_fma_f32 v[64:65], v[74:75], v[122:123], v[80:81] op_sel_hi:[0,1,1]
	s_waitcnt vmcnt(0)
	v_readfirstlane_b32 s8, v96
	v_readfirstlane_b32 s28, v97
	s_bfe_u32 s29, s8, 0x100010
	s_bfe_u32 s33, s28, 0x100010
	s_lshl_b32 s29, s29, 2
	v_pk_fma_f32 v[62:63], v[74:75], v[78:79], v[62:63] op_sel_hi:[0,1,1]
	s_lshl_b32 s33, s33, 2
	s_add_i32 s29, s36, s29
	v_pk_fma_f32 v[96:97], v[74:75], v[134:135], v[64:65] op_sel:[1,0,0]
	v_pk_fma_f32 v[134:135], v[74:75], v[76:77], v[62:63] op_sel:[1,0,0]
	s_add_i32 s33, s36, s33
	v_mov_b32_e32 v62, s29
	v_mov_b32_e32 v63, s33
	ds_read_b32 v62, v62
	ds_read_b32 v64, v63
	s_lshl_b32 s8, s8, 11
	s_lshl_b32 s28, s28, 11
	s_and_b32 s8, s8, 0x7fff800
	s_waitcnt lgkmcnt(1)
	v_ashrrev_i32_e32 v63, 31, v62
	s_waitcnt lgkmcnt(0)
	v_ashrrev_i32_e32 v65, 31, v64
	v_lshlrev_b64 v[62:63], 19, v[62:63]
	v_lshlrev_b64 v[64:65], 19, v[64:65]
	v_lshl_add_u64 v[62:63], s[2:3], 0, v[62:63]
	v_lshl_add_u64 v[64:65], s[2:3], 0, v[64:65]
	v_lshl_add_u64 v[62:63], v[62:63], 0, s[8:9]
	s_and_b32 s8, s28, 0x7fff800
	v_pk_fma_f32 v[80:81], v[74:75], v[124:125], v[82:83] op_sel_hi:[0,1,1]
	v_pk_fma_f32 v[82:83], v[74:75], v[126:127], v[84:85] op_sel_hi:[0,1,1]
	v_lshl_add_u64 v[62:63], v[62:63], 0, v[18:19]
	v_lshl_add_u64 v[64:65], v[64:65], 0, s[8:9]
	v_pk_fma_f32 v[68:69], v[74:75], v[68:69], v[70:71] op_sel_hi:[0,1,1]
	v_pk_fma_f32 v[70:71], v[74:75], v[128:129], v[72:73] op_sel_hi:[0,1,1]
	v_pk_fma_f32 v[72:73], v[74:75], v[130:131], v[86:87] op_sel_hi:[0,1,1]
	v_pk_fma_f32 v[122:123], v[74:75], v[136:137], v[80:81] op_sel:[1,0,0]
	v_pk_fma_f32 v[124:125], v[74:75], v[138:139], v[82:83] op_sel:[1,0,0]
	global_load_dwordx2 v[136:137], v[62:63], off offset:1024
	global_load_dwordx2 v[138:139], v[62:63], off offset:1536
	v_lshl_add_u64 v[62:63], v[64:65], 0, v[18:19]
	v_pk_fma_f32 v[84:85], v[74:75], v[132:133], v[88:89] op_sel_hi:[0,1,1]
	v_pk_fma_f32 v[128:129], v[74:75], v[140:141], v[70:71] op_sel:[1,0,0]
	v_pk_fma_f32 v[130:131], v[74:75], v[142:143], v[72:73] op_sel:[1,0,0]
	global_load_dwordx2 v[140:141], v[62:63], off offset:1024
	global_load_dwordx2 v[142:143], v[62:63], off offset:1536
	v_pk_fma_f32 v[132:133], v[74:75], v[144:145], v[84:85] op_sel:[1,0,0]
	global_load_dwordx2 v[144:145], v56, s[24:25] offset:16
	v_pk_fma_f32 v[126:127], v[74:75], v[66:67], v[68:69] op_sel:[1,0,0]
	global_load_dwordx4 v[62:65], v[54:55], off offset:16
	global_load_dwordx4 v[66:69], v59, s[26:27]
	global_load_dwordx4 v[70:73], v[48:49], off
	global_load_dwordx4 v[74:77], v[48:49], off offset:2048
	global_load_dwordx4 v[78:81], v59, s[26:27] offset:16
	s_nop 0
	global_load_dwordx4 v[52:55], v[52:53], off offset:16
	s_nop 0
	global_load_dwordx4 v[82:85], v60, s[26:27] offset:16
	global_load_dwordx4 v[86:89], v60, s[26:27]
	global_load_dwordx2 v[148:149], v56, s[24:25] offset:24
	v_cvt_pk_f32_fp8_sdwa v[100:101], v90 src0_sel:WORD_1
	v_cvt_pk_f32_fp8_e32 v[102:103], v91
	v_cvt_pk_f32_fp8_sdwa v[90:91], v91 src0_sel:WORD_1
	v_cvt_pk_f32_fp8_e32 v[112:113], v92
	v_cvt_pk_f32_fp8_sdwa v[114:115], v92 src0_sel:WORD_1
	v_cvt_pk_f32_fp8_e32 v[116:117], v93
	v_cvt_pk_f32_fp8_sdwa v[92:93], v93 src0_sel:WORD_1
	v_cvt_pk_f32_fp8_e32 v[118:119], v94
	v_cvt_pk_f32_fp8_sdwa v[120:121], v94 src0_sel:WORD_1
	v_cvt_pk_f32_fp8_e32 v[146:147], v95
	v_cvt_pk_f32_fp8_sdwa v[94:95], v95 src0_sel:WORD_1
	global_store_dwordx4 v[48:49], v[14:17], off offset:-4096
	global_store_dwordx4 v[50:51], v[10:13], off offset:16
	global_store_dwordx4 v[50:51], v[6:9], off offset:2048
	global_store_dwordx4 v[50:51], v[2:5], off offset:2064
	s_add_u32 s28, s30, 0x18000
	s_addc_u32 s29, s31, 0
	s_add_u32 s30, s30, 0x1a000
	s_addc_u32 s31, s31, 0
	s_add_i32 s8, s4, 0x800
	s_add_u32 s6, s6, 0x10000
	s_addc_u32 s7, s7, 0
	s_cmpk_lt_i32 s4, 0x1800
	s_mov_b32 s4, s8
	s_waitcnt vmcnt(17)
	v_cvt_pk_f32_fp8_e32 v[50:51], v136
	v_cvt_pk_f32_fp8_sdwa v[150:151], v136 src0_sel:WORD_1
	v_cvt_pk_f32_fp8_e32 v[152:153], v137
	v_cvt_pk_f32_fp8_sdwa v[136:137], v137 src0_sel:WORD_1
	s_waitcnt vmcnt(16)
	v_cvt_pk_f32_fp8_e32 v[154:155], v138
	v_cvt_pk_f32_fp8_sdwa v[156:157], v138 src0_sel:WORD_1
	v_cvt_pk_f32_fp8_e32 v[158:159], v139
	v_cvt_pk_f32_fp8_sdwa v[138:139], v139 src0_sel:WORD_1
	s_waitcnt vmcnt(15)
	v_cvt_pk_f32_fp8_e32 v[160:161], v140
	v_cvt_pk_f32_fp8_sdwa v[162:163], v140 src0_sel:WORD_1
	v_cvt_pk_f32_fp8_e32 v[164:165], v141
	v_cvt_pk_f32_fp8_sdwa v[140:141], v141 src0_sel:WORD_1
	s_waitcnt vmcnt(14)
	v_cvt_pk_f32_fp8_e32 v[166:167], v142
	v_cvt_pk_f32_fp8_sdwa v[168:169], v142 src0_sel:WORD_1
	v_cvt_pk_f32_fp8_e32 v[170:171], v143
	v_cvt_pk_f32_fp8_sdwa v[142:143], v143 src0_sel:WORD_1
	s_waitcnt vmcnt(13)
	v_pk_fma_f32 v[96:97], v[144:145], v[98:99], v[96:97] op_sel_hi:[0,1,1]
	v_pk_fma_f32 v[98:99], v[144:145], v[100:101], v[122:123] op_sel_hi:[0,1,1]
	v_pk_fma_f32 v[100:101], v[144:145], v[102:103], v[124:125] op_sel_hi:[0,1,1]
	v_pk_fma_f32 v[90:91], v[144:145], v[90:91], v[126:127] op_sel_hi:[0,1,1]
	v_pk_fma_f32 v[102:103], v[144:145], v[104:105], v[128:129] op_sel_hi:[0,1,1]
	v_pk_fma_f32 v[104:105], v[144:145], v[106:107], v[130:131] op_sel_hi:[0,1,1]
	v_pk_fma_f32 v[106:107], v[144:145], v[108:109], v[132:133] op_sel_hi:[0,1,1]
	v_pk_fma_f32 v[108:109], v[144:145], v[110:111], v[134:135] op_sel_hi:[0,1,1]
	v_pk_fma_f32 v[96:97], v[144:145], v[112:113], v[96:97] op_sel:[1,0,0]
	v_pk_fma_f32 v[98:99], v[144:145], v[114:115], v[98:99] op_sel:[1,0,0]
	v_pk_fma_f32 v[100:101], v[144:145], v[116:117], v[100:101] op_sel:[1,0,0]
	v_pk_fma_f32 v[90:91], v[144:145], v[92:93], v[90:91] op_sel:[1,0,0]
	v_pk_fma_f32 v[92:93], v[144:145], v[118:119], v[102:103] op_sel:[1,0,0]
	v_pk_fma_f32 v[102:103], v[144:145], v[120:121], v[104:105] op_sel:[1,0,0]
	v_pk_fma_f32 v[104:105], v[144:145], v[146:147], v[106:107] op_sel:[1,0,0]
	v_pk_fma_f32 v[94:95], v[144:145], v[94:95], v[108:109] op_sel:[1,0,0]
	s_waitcnt vmcnt(4)
; __device__ __forceinline__ float row_rstd(const Row& r) {
;     float s = 0.f;
; #pragma unroll
;     for (int j = 0; j < 4; ++j)
; #pragma unroll
;         for (int q = 0; q < 8; ++q) s += r.v[j][q] * r.v[j][q];
;     return rsqrtf(wave_sum(s) * (1.0f / DM) + EPS);
; }
; __device__ __forceinline__ void combine_phase(CArgs& A, int l, const float* xin, LAS unsigned char* lds, int vcu, int G) {
;     ...
;             CB_ACC(rb, 6)
; #pragma unroll
;             for (int j = 0; j < 2; ++j)
; #pragma unroll
;                 for (int q4 = 0; q4 < 2; ++q4)
; #pragma unroll
;                     for (int q = 0; q < 4; ++q) x.v[2 * hh + j][4 * q4 + q] = xv[j][q4][q] + gv[j][q4][q] * y[j][4 * q4 + q];
;             asm volatile("" ::: "memory");
;         }
;     ...
;         if (!lastl) {
;             row_store_f32(x, X + (size_t)t * DM, lane);
;             row_norm_mod_store(x, A.in[I_GMIX] + (size_t)(l + 1) * DM, mod_ptr(A, l + 1, b, 0), mod_ptr(A, l + 1, b, 1), H + (size_t)t * DM, lane, A.ws + WS_H8 + (size_t)t * DM);
	v_pk_fma_f32 v[50:51], v[148:149], v[50:51], v[96:97] op_sel_hi:[0,1,1]
	v_pk_fma_f32 v[96:97], v[148:149], v[150:151], v[98:99] op_sel_hi:[0,1,1]
	v_pk_fma_f32 v[98:99], v[148:149], v[152:153], v[100:101] op_sel_hi:[0,1,1]
	v_pk_fma_f32 v[90:91], v[148:149], v[136:137], v[90:91] op_sel_hi:[0,1,1]
	v_pk_fma_f32 v[92:93], v[148:149], v[154:155], v[92:93] op_sel_hi:[0,1,1]
	v_pk_fma_f32 v[100:101], v[148:149], v[156:157], v[102:103] op_sel_hi:[0,1,1]
	v_pk_fma_f32 v[102:103], v[148:149], v[158:159], v[104:105] op_sel_hi:[0,1,1]
	v_pk_fma_f32 v[94:95], v[148:149], v[138:139], v[94:95] op_sel_hi:[0,1,1]
	v_pk_fma_f32 v[50:51], v[148:149], v[160:161], v[50:51] op_sel:[1,0,0]
	v_pk_fma_f32 v[96:97], v[148:149], v[162:163], v[96:97] op_sel:[1,0,0]
	v_pk_fma_f32 v[98:99], v[148:149], v[164:165], v[98:99] op_sel:[1,0,0]
	v_pk_fma_f32 v[90:91], v[148:149], v[140:141], v[90:91] op_sel:[1,0,0]
	v_pk_fma_f32 v[92:93], v[148:149], v[166:167], v[92:93] op_sel:[1,0,0]
	v_pk_fma_f32 v[100:101], v[148:149], v[168:169], v[100:101] op_sel:[1,0,0]
	v_pk_fma_f32 v[102:103], v[148:149], v[170:171], v[102:103] op_sel:[1,0,0]
	v_pk_fma_f32 v[94:95], v[148:149], v[142:143], v[94:95] op_sel:[1,0,0]
	v_pk_fma_f32 v[66:67], v[66:67], v[50:51], v[70:71]
	v_pk_fma_f32 v[68:69], v[68:69], v[96:97], v[72:73]
	v_pk_fma_f32 v[62:63], v[78:79], v[98:99], v[62:63]
	v_pk_fma_f32 v[64:65], v[80:81], v[90:91], v[64:65]
	v_pk_fma_f32 v[70:71], v[86:87], v[92:93], v[74:75]
	v_pk_fma_f32 v[72:73], v[88:89], v[100:101], v[76:77]
	v_pk_fma_f32 v[50:51], v[82:83], v[102:103], v[52:53]
	v_pk_fma_f32 v[52:53], v[84:85], v[94:95], v[54:55]
	global_store_dwordx4 v[48:49], v[66:69], off
	global_store_dwordx4 v[48:49], v[62:65], off offset:16
	global_store_dwordx4 v[48:49], v[70:73], off offset:2048
	global_store_dwordx4 v[48:49], v[50:53], off offset:2064
	global_load_dwordx4 v[74:77], v[20:21], off offset:16
	global_load_dwordx4 v[78:81], v[20:21], off
	global_load_dwordx4 v[82:85], v57, s[28:29] offset:16
	global_load_dwordx4 v[86:89], v57, s[28:29]
	global_load_dwordx4 v[90:93], v57, s[30:31] offset:16
	global_load_dwordx4 v[94:97], v57, s[30:31]
	global_load_dwordx4 v[98:101], v[22:23], off offset:16
	global_load_dwordx4 v[102:105], v[22:23], off
	global_load_dwordx4 v[106:109], v58, s[28:29] offset:16
	global_load_dwordx4 v[110:113], v58, s[28:29]
	global_load_dwordx4 v[114:117], v58, s[30:31] offset:16
	global_load_dwordx4 v[118:121], v58, s[30:31]
	global_load_dwordx4 v[122:125], v[24:25], off offset:16
	global_load_dwordx4 v[126:129], v[24:25], off
	global_load_dwordx4 v[130:133], v59, s[28:29] offset:16
	global_load_dwordx4 v[134:137], v59, s[28:29]
	global_load_dwordx4 v[138:141], v59, s[30:31] offset:16
	global_load_dwordx4 v[142:145], v59, s[30:31]
	global_load_dwordx4 v[146:149], v[26:27], off offset:16
	global_load_dwordx4 v[150:153], v[26:27], off
	global_load_dwordx4 v[154:157], v60, s[28:29] offset:16
	global_load_dwordx4 v[158:161], v60, s[28:29]
	global_load_dwordx4 v[162:165], v60, s[30:31] offset:16
	global_load_dwordx4 v[166:169], v60, s[30:31]
	v_pk_mul_f32 v[48:49], v[66:67], v[66:67]
	v_pk_mul_f32 v[54:55], v[68:69], v[68:69]
	v_add_f32_e32 v48, v182, v48
	v_add_f32_e32 v48, v49, v48
	v_add_f32_e32 v48, v54, v48
	v_pk_mul_f32 v[170:171], v[62:63], v[62:63]
	v_add_f32_e32 v48, v55, v48
	v_add_f32_e32 v48, v170, v48
	v_pk_mul_f32 v[172:173], v[64:65], v[64:65]
	v_add_f32_e32 v48, v171, v48
	v_add_f32_e32 v48, v172, v48
	v_pk_mul_f32 v[174:175], v[70:71], v[70:71]
	v_add_f32_e32 v48, v173, v48
	v_add_f32_e32 v48, v174, v48
	v_pk_mul_f32 v[176:177], v[72:73], v[72:73]
	v_add_f32_e32 v48, v175, v48
	v_add_f32_e32 v48, v176, v48
	v_pk_mul_f32 v[178:179], v[50:51], v[50:51]
	v_add_f32_e32 v48, v177, v48
	v_add_f32_e32 v48, v178, v48
	v_pk_mul_f32 v[180:181], v[52:53], v[52:53]
	v_add_f32_e32 v48, v179, v48
	v_add_f32_e32 v48, v180, v48
	v_add_f32_e32 v48, v181, v48
	s_nop 1
	v_add_f32_dpp v48, v48, v48 quad_perm:[1,0,3,2] row_mask:0xf bank_mask:0xf bound_ctrl:1
	s_nop 1
	v_add_f32_dpp v48, v48, v48 quad_perm:[2,3,0,1] row_mask:0xf bank_mask:0xf bound_ctrl:1
	s_nop 1
	v_add_f32_dpp v48, v48, v48 row_half_mirror row_mask:0xf bank_mask:0xf bound_ctrl:1
	s_nop 1
	v_add_f32_dpp v48, v48, v48 row_mirror row_mask:0xf bank_mask:0xf bound_ctrl:1
	s_nop 0
	v_readlane_b32 s8, v48, 16
	v_readlane_b32 s26, v48, 48
	v_readlane_b32 s24, v48, 0
	v_readlane_b32 s25, v48, 32
	v_mov_b32_e32 v48, s8
	v_mov_b32_e32 v49, s26
	v_pk_add_f32 v[48:49], s[24:25], v[48:49]
	s_nop 0
	v_add_f32_e32 v48, v48, v49
	v_fmamk_f32 v48, v48, 0x3a000000, v61
	v_mul_f32_e32 v49, 0x4b800000, v48
	v_cmp_gt_f32_e32 vcc, s39, v48
	s_nop 1
	v_cndmask_b32_e32 v48, v48, v49, vcc
	v_rsq_f32_e32 v48, v48
	s_nop 0
	v_mul_f32_e32 v49, 0x45800000, v48
	v_cndmask_b32_e32 v48, v48, v49, vcc
	v_mul_f32_e32 v14, v14, v48
	v_mul_f32_e32 v15, v15, v48
	v_mul_f32_e32 v16, v16, v48
	v_mul_f32_e32 v17, v17, v48
	v_mul_f32_e32 v10, v10, v48
	v_mul_f32_e32 v11, v11, v48
	v_mul_f32_e32 v13, v13, v48
	v_mul_f32_e32 v12, v12, v48
	v_mul_f32_e32 v6, v6, v48
	v_mul_f32_e32 v7, v7, v48
	v_mul_f32_e32 v8, v8, v48
	v_mul_f32_e32 v9, v9, v48
	v_mul_f32_e32 v2, v2, v48
	v_mul_f32_e32 v3, v3, v48
	v_mul_f32_e32 v4, v4, v48
	v_mul_f32_e32 v5, v5, v48
	v_mul_f32_e32 v49, v66, v48
	v_mul_f32_e32 v54, v67, v48
	v_mul_f32_e32 v55, v68, v48
	v_mul_f32_e32 v66, v69, v48
	v_mul_f32_e32 v62, v62, v48
	v_mul_f32_e32 v63, v63, v48
	v_mul_f32_e32 v64, v64, v48
	v_mul_f32_e32 v65, v65, v48
	v_mul_f32_e32 v67, v70, v48
	v_mul_f32_e32 v68, v71, v48
	v_mul_f32_e32 v69, v72, v48
	v_mul_f32_e32 v70, v73, v48
	v_mul_f32_e32 v50, v50, v48
	v_mul_f32_e32 v51, v51, v48
	v_mul_f32_e32 v52, v52, v48
	v_mul_f32_e32 v48, v53, v48
	s_waitcnt vmcnt(22)
; __device__ __forceinline__ void row_norm_mod_store(const Row& x, const float* g, ModPtr sh, ModPtr sc, bf16* hrow, int lane, unsigned char* h8row = nullptr) {
;     const float rstd = row_rstd(x);
;     Row o;
; #pragma unroll
;     for (int j = 0; j < 4; ++j) { const int c0 = 512 * j + 8 * lane;
; #pragma unroll
;         for (int q4 = 0; q4 < 2; ++q4) { const int c = c0 + 4 * q4;
;             const f32x4 gv = *(const f32x4*)(g + c), sa = *(const f32x4*)(sh.acc + c), ca = *(const f32x4*)(sc.acc + c);
; #pragma unroll
;             for (int q = 0; q < 4; ++q) o.v[j][4 * q4 + q] = (x.v[j][4 * q4 + q] * rstd * gv[q]) * (1.0f + ca[q]) + sa[q]; }
;         asm volatile("" ::: "memory"); }
;     if (hrow) row_store_bf16(o, hrow, lane);
;     if (h8row) {
; #pragma unroll
;         for (int j = 0; j < 4; ++j) *(u32x2*)(h8row + 512 * j + 8 * lane) = pack8_fp8((f32x4){o.v[j][0], o.v[j][1], o.v[j][2], o.v[j][3]}, (f32x4){o.v[j][4], o.v[j][5], o.v[j][6], o.v[j][7]}); }
; }
	v_mul_f32_e32 v14, v78, v14
	s_waitcnt vmcnt(18)
	v_add_f32_e32 v53, 1.0, v94
	v_mul_f32_e32 v15, v79, v15
	v_add_f32_e32 v71, 1.0, v95
	v_mul_f32_e32 v16, v80, v16
	v_add_f32_e32 v72, 1.0, v96
	v_mul_f32_e32 v17, v81, v17
	v_add_f32_e32 v73, 1.0, v97
	v_mul_f32_e32 v10, v74, v10
	v_add_f32_e32 v74, 1.0, v90
	v_mul_f32_e32 v11, v75, v11
	v_add_f32_e32 v75, 1.0, v91
	v_mul_f32_e32 v13, v77, v13
	v_add_f32_e32 v77, 1.0, v93
	v_mul_f32_e32 v12, v76, v12
	v_add_f32_e32 v76, 1.0, v92
	v_fma_f32 v14, v53, v14, v86
	v_fma_f32 v15, v71, v15, v87
	v_fma_f32 v16, v72, v16, v88
	v_fmac_f32_e32 v89, v73, v17
	v_fma_f32 v10, v74, v10, v82
	v_fma_f32 v11, v75, v11, v83
	v_fmac_f32_e32 v85, v77, v13
	s_waitcnt vmcnt(16)
	v_mul_f32_e32 v6, v102, v6
	s_waitcnt vmcnt(12)
	v_add_f32_e32 v13, 1.0, v118
	v_mul_f32_e32 v7, v103, v7
	v_add_f32_e32 v17, 1.0, v119
	v_mul_f32_e32 v8, v104, v8
	v_add_f32_e32 v53, 1.0, v120
	v_mul_f32_e32 v9, v105, v9
	v_add_f32_e32 v71, 1.0, v121
	v_mul_f32_e32 v2, v2, v98
	v_add_f32_e32 v72, 1.0, v114
	v_mul_f32_e32 v3, v3, v99
	v_add_f32_e32 v73, 1.0, v115
	v_mul_f32_e32 v4, v4, v100
	v_add_f32_e32 v74, 1.0, v116
	v_mul_f32_e32 v5, v5, v101
	v_add_f32_e32 v75, 1.0, v117
	v_fma_f32 v12, v76, v12, v84
	v_fma_f32 v6, v6, v13, v110
	v_fma_f32 v7, v7, v17, v111
	v_fma_f32 v8, v8, v53, v112
	v_fmac_f32_e32 v113, v9, v71
	v_fma_f32 v9, v2, v72, v106
	v_fma_f32 v13, v3, v73, v107
	v_fma_f32 v17, v4, v74, v108
	v_fmac_f32_e32 v109, v5, v75
	s_waitcnt vmcnt(10)
	v_mul_f32_e32 v49, v49, v126
	s_waitcnt vmcnt(6)
	v_add_f32_e32 v53, 1.0, v142
	v_mul_f32_e32 v54, v54, v127
	v_add_f32_e32 v71, 1.0, v143
	v_mul_f32_e32 v55, v55, v128
	v_add_f32_e32 v72, 1.0, v144
	v_mul_f32_e32 v62, v62, v122
	v_add_f32_e32 v74, 1.0, v138
	v_mul_f32_e32 v63, v63, v123
	v_add_f32_e32 v75, 1.0, v139
	v_mul_f32_e32 v64, v64, v124
	v_add_f32_e32 v76, 1.0, v140
	v_cvt_pk_fp8_f32 v36, v14, v15
	v_cvt_pk_fp8_f32 v37, v10, v11
	v_cvt_pk_bf16_f32 v2, v14, v15
	v_cvt_pk_bf16_f32 v3, v16, v89
	v_cvt_pk_bf16_f32 v4, v10, v11
	v_fma_f32 v10, v49, v53, v134
	v_fma_f32 v11, v54, v71, v135
	v_fma_f32 v14, v55, v72, v136
	v_fma_f32 v15, v62, v74, v130
	v_fma_f32 v49, v63, v75, v131
	v_fma_f32 v53, v64, v76, v132
	s_waitcnt vmcnt(4)
	v_mul_f32_e32 v54, v67, v150
	s_waitcnt vmcnt(0)
	v_add_f32_e32 v55, 1.0, v166
	v_mul_f32_e32 v62, v68, v151
	v_add_f32_e32 v63, 1.0, v167
	v_mul_f32_e32 v64, v69, v152
	v_mul_f32_e32 v50, v50, v146
	v_add_f32_e32 v68, 1.0, v162
	v_mul_f32_e32 v51, v51, v147
	v_add_f32_e32 v69, 1.0, v163
	v_cvt_pk_fp8_f32 v38, v6, v7
	v_cvt_pk_fp8_f32 v39, v9, v13
	v_cvt_pk_bf16_f32 v5, v12, v85
	v_cvt_pk_fp8_f32 v40, v10, v11
	v_cvt_pk_fp8_f32 v41, v15, v49
	v_cvt_pk_bf16_f32 v2, v6, v7
	v_cvt_pk_bf16_f32 v3, v8, v113
	v_cvt_pk_bf16_f32 v4, v9, v13
	v_fma_f32 v6, v54, v55, v158
	v_fma_f32 v7, v62, v63, v159
	v_fma_f32 v13, v50, v68, v154
	v_fma_f32 v50, v51, v69, v155
	v_cvt_pk_fp8_f32 v42, v6, v7
	v_cvt_pk_fp8_f32 v43, v13, v50
	v_mul_f32_e32 v66, v66, v129
	v_add_f32_e32 v73, 1.0, v145
	v_mul_f32_e32 v65, v65, v125
	v_add_f32_e32 v77, 1.0, v141
	v_cvt_pk_fp8_f32 v36, v16, v89 op_sel:[0,0,1]
	v_cvt_pk_fp8_f32 v37, v12, v85 op_sel:[0,0,1]
	v_fmac_f32_e32 v137, v66, v73
	v_fmac_f32_e32 v133, v65, v77
	v_add_f32_e32 v65, 1.0, v168
	v_mul_f32_e32 v66, v70, v153
	v_add_f32_e32 v67, 1.0, v169
	v_mul_f32_e32 v52, v52, v148
	v_add_f32_e32 v70, 1.0, v164
	v_mul_f32_e32 v48, v48, v149
	v_add_f32_e32 v71, 1.0, v165
	v_cvt_pk_fp8_f32 v38, v8, v113 op_sel:[0,0,1]
	v_cvt_pk_fp8_f32 v39, v17, v109 op_sel:[0,0,1]
	v_cvt_pk_bf16_f32 v5, v17, v109
	v_fma_f32 v9, v64, v65, v160
	v_fmac_f32_e32 v161, v66, v67
	v_fma_f32 v51, v52, v70, v156
	v_fmac_f32_e32 v157, v48, v71
	v_cvt_pk_fp8_f32 v40, v14, v137 op_sel:[0,0,1]
	v_cvt_pk_fp8_f32 v41, v53, v133 op_sel:[0,0,1]
	v_cvt_pk_fp8_f32 v42, v9, v161 op_sel:[0,0,1]
	v_cvt_pk_fp8_f32 v43, v51, v157 op_sel:[0,0,1]
	v_cvt_pk_bf16_f32 v2, v10, v11
	v_cvt_pk_bf16_f32 v3, v14, v137
	v_cvt_pk_bf16_f32 v4, v15, v49
	v_cvt_pk_bf16_f32 v5, v53, v133
	s_nop 1
	v_cvt_pk_bf16_f32 v2, v6, v7
	v_cvt_pk_bf16_f32 v3, v9, v161
	v_cvt_pk_bf16_f32 v4, v13, v50
	v_cvt_pk_bf16_f32 v5, v51, v157
	global_store_dwordx2 v[44:45], v[36:37], off
	global_store_dwordx2 v[44:45], v[38:39], off offset:512
	global_store_dwordx2 v[44:45], v[40:41], off offset:1024
	global_store_dwordx2 v[44:45], v[42:43], off offset:1536
	s_cbranch_scc1 .LBB0_1734
	v_readlane_b32 s24, v255, 0
	v_readlane_b32 s25, v255, 1
